# attention K-tile LDS swizzle made conflict-free ((row>>1)&7 key); ret_gate gains staged in wave-private LDS with counted vmcnt waits; plus v21 changes
# speedup vs baseline: 1.0021x; 1.0021x over previous
.LBB0_527:
	s_cmp_lt_i32 s92, 6
	s_cselect_b64 s[4:5], -1, 0
	s_cmp_gt_i32 s93, 5
	s_cselect_b64 s[6:7], -1, 0
	s_and_b64 s[4:5], s[4:5], s[6:7]
	s_andn2_b64 vcc, exec, s[4:5]
	s_cbranch_vccnz .LBB0_581
	s_lshl_b32 s3, s89, 3
	s_add_i32 s6, s3, s88
	s_cmpk_gt_i32 s6, 0x43ff
	s_mov_b32 s10, 13
	s_mov_b32 s4, 14
	s_cbranch_scc1 .LBB0_531
	s_add_u32 s3, s26, 0x2a500000
	s_addc_u32 s15, s27, 0
	s_ashr_i32 s11, s10, 31
	s_lshl_b32 s8, s34, 3
	s_lshl_b64 s[10:11], s[10:11], 3
	s_add_u32 s12, s0, s10
	s_addc_u32 s13, s1, s11
	s_add_u32 s16, s26, 0x3d700000
	s_addc_u32 s17, s27, 0
	s_ashr_i32 s7, s6, 31
	s_lshl_b64 s[18:19], s[6:7], 12
	s_add_u32 s20, s16, s18
	s_addc_u32 s21, s17, s19
	s_add_u32 s22, s26, 0x41b00000
	s_waitcnt vmcnt(0)
	v_lshlrev_b32_e32 v2, 3, v250
	s_addc_u32 s23, s27, 0
	v_lshlrev_b32_e32 v1, 5, v250
	v_and_b32_e32 v2, 0x78, v2
	s_movk_i32 s5, 0xfe00
	s_add_u32 s28, s22, s18
	v_and_or_b32 v146, v1, s5, v2
	s_addc_u32 s29, s23, s19
	s_lshl_b64 s[10:11], s[6:7], 13
	v_ashrrev_i32_e32 v147, 31, v146
	s_add_u32 s10, s3, s10
	s_addc_u32 s11, s15, s11
	v_lshlrev_b64 v[2:3], 1, v[146:147]
	v_lshl_add_u64 v[4:5], s[10:11], 0, v[2:3]
	s_movk_i32 s7, 0x1000
	s_mov_b64 s[10:11], 0x1000
	v_lshl_add_u64 v[10:11], s[20:21], 0, v[2:3]
	v_add_co_u32_e32 v12, vcc, s7, v4
	v_lshl_add_u64 v[6:7], v[4:5], 0, s[10:11]
	v_lshl_add_u64 v[8:9], s[28:29], 0, v[2:3]
	global_load_dwordx4 v[34:37], v[4:5], off offset:768
	global_load_dwordx4 v[74:77], v[4:5], off offset:512
	global_load_dwordx4 v[78:81], v[6:7], off offset:512
	global_load_dwordx4 v[82:85], v[6:7], off offset:256
	global_load_dwordx4 v[106:109], v[8:9], off offset:512
	global_load_dwordx4 v[122:125], v[8:9], off offset:256
	global_load_dwordx4 v[118:121], v[10:11], off offset:512
	global_load_dwordx4 v[126:129], v[10:11], off offset:256
	v_addc_co_u32_e32 v13, vcc, 0, v5, vcc
	global_load_dwordx4 v[110:113], v[10:11], off offset:768
	global_load_dwordx4 v[94:97], v[12:13], off
	global_load_dwordx4 v[86:89], v[4:5], off offset:256
	global_load_dwordx4 v[90:93], v[4:5], off
	global_load_dwordx4 v[38:41], v[6:7], off offset:768
	global_load_dwordx4 v[130:133], v[8:9], off
	global_load_dwordx4 v[114:117], v[8:9], off offset:768
	global_load_dwordx4 v[134:137], v[10:11], off
	s_ashr_i32 s5, s4, 31
	s_lshl_b64 s[4:5], s[4:5], 3
	s_add_u32 s4, s0, s4
	s_addc_u32 s5, s1, s5
	s_load_dwordx2 s[20:21], s[12:13], 0x0
	s_load_dwordx2 s[28:29], s[4:5], 0x0
	s_add_u32 s4, s26, s18
	s_addc_u32 s5, s27, s19
	v_lshl_add_u64 v[148:149], s[16:17], 0, v[2:3]
	v_lshl_add_u64 v[150:151], s[22:23], 0, v[2:3]
	v_lshlrev_b64 v[4:5], 2, v[146:147]
	v_lshl_add_u64 v[2:3], s[4:5], 0, v[2:3]
	s_mov_b64 s[4:5], 0x45f00000
	s_ashr_i32 s9, s8, 31
	s_waitcnt lgkmcnt(0)
	v_lshl_add_u64 v[152:153], s[20:21], 0, v[4:5]
	v_lshl_add_u64 v[154:155], s[28:29], 0, v[4:5]
	v_lshl_add_u64 v[156:157], v[2:3], 0, s[4:5]
	s_lshl_b64 s[12:13], s[8:9], 12
	s_mov_b32 s14, 0x3b000000
	v_mov_b32_e32 v1, 0x358637bd
	s_mov_b32 s9, 0xf800000
	v_mov_b32_e32 v171, 0x260
	v_lshlrev_b32_e32 v242, 4, v250
	s_lshl_b32 s98, s88, 14
	v_add_u32_e32 v242, s98, v242
	global_load_dwordx4 v[2:5], v[152:153], off
	global_load_dwordx4 v[6:9], v[152:153], off offset:16
	global_load_dwordx4 v[10:13], v[152:153], off offset:512
	global_load_dwordx4 v[14:17], v[152:153], off offset:528
	global_load_dwordx4 v[18:21], v[152:153], off offset:1024
	global_load_dwordx4 v[22:25], v[152:153], off offset:1040
	global_load_dwordx4 v[26:29], v[152:153], off offset:1536
	global_load_dwordx4 v[30:33], v[152:153], off offset:1552
	global_load_dwordx4 v[42:45], v[154:155], off
	global_load_dwordx4 v[46:49], v[154:155], off offset:16
	global_load_dwordx4 v[50:53], v[154:155], off offset:512
	global_load_dwordx4 v[54:57], v[154:155], off offset:528
	global_load_dwordx4 v[58:61], v[154:155], off offset:1024
	global_load_dwordx4 v[62:65], v[154:155], off offset:1040
	global_load_dwordx4 v[66:69], v[154:155], off offset:1536
	global_load_dwordx4 v[70:73], v[154:155], off offset:1552
	s_waitcnt vmcnt(0)
	ds_write_b128 v242, v[2:5]
	ds_write_b128 v242, v[6:9] offset:1024
	ds_write_b128 v242, v[10:13] offset:2048
	ds_write_b128 v242, v[14:17] offset:3072
	ds_write_b128 v242, v[18:21] offset:4096
	ds_write_b128 v242, v[22:25] offset:5120
	ds_write_b128 v242, v[26:29] offset:6144
	ds_write_b128 v242, v[30:33] offset:7168
	ds_write_b128 v242, v[42:45] offset:8192
	ds_write_b128 v242, v[46:49] offset:9216
	ds_write_b128 v242, v[50:53] offset:10240
	ds_write_b128 v242, v[54:57] offset:11264
	ds_write_b128 v242, v[58:61] offset:12288
	ds_write_b128 v242, v[62:65] offset:13312
	ds_write_b128 v242, v[66:69] offset:14336
	ds_write_b128 v242, v[70:73] offset:15360
	s_waitcnt lgkmcnt(0)
.LBB0_530:
	s_add_i32 s6, s6, s8
	s_min_i32 s4, s6, 0x43ff
	s_ashr_i32 s5, s4, 31
	s_lshl_b64 s[16:17], s[4:5], 12
	s_lshl_b64 s[4:5], s[4:5], 13
	s_add_u32 s4, s3, s4
	s_addc_u32 s5, s15, s5
	v_lshl_add_u64 v[66:67], v[146:147], 1, s[4:5]
	v_add_co_u32_e32 v24, vcc, s7, v66
	v_lshl_add_u64 v[22:23], v[148:149], 0, s[16:17]
	v_lshl_add_u64 v[30:31], v[150:151], 0, s[16:17]
	v_lshl_add_u64 v[68:69], v[66:67], 0, s[10:11]
	v_addc_co_u32_e32 v25, vcc, 0, v67, vcc
	global_load_dwordx4 v[2:5], v[22:23], off
	global_load_dwordx4 v[6:9], v[30:31], off
	global_load_dwordx4 v[46:49], v[66:67], off
	global_load_dwordx4 v[42:45], v[24:25], off
	global_load_dwordx4 v[10:13], v[22:23], off offset:256
	global_load_dwordx4 v[18:21], v[30:31], off offset:256
	global_load_dwordx4 v[54:57], v[66:67], off offset:256
	global_load_dwordx4 v[50:53], v[68:69], off offset:256
	global_load_dwordx4 v[14:17], v[22:23], off offset:512
	global_load_dwordx4 v[26:29], v[30:31], off offset:512
	global_load_dwordx4 v[62:65], v[66:67], off offset:512
	global_load_dwordx4 v[58:61], v[68:69], off offset:512
	s_nop 0
	global_load_dwordx4 v[22:25], v[22:23], off offset:768
	s_nop 0
	global_load_dwordx4 v[30:33], v[30:31], off offset:768
	s_nop 0
	global_load_dwordx4 v[70:73], v[66:67], off offset:768
	s_nop 0
	global_load_dwordx4 v[66:69], v[68:69], off offset:768
	s_nop 0
	ds_read_b128 v[142:145], v242
	ds_read_b128 v[138:141], v242 offset:1024
	ds_read_b128 v[102:105], v242 offset:8192
	ds_read_b128 v[98:101], v242 offset:9216
	s_waitcnt vmcnt(20)
	v_lshlrev_b32_e32 v158, 16, v93
	s_waitcnt vmcnt(21)
	v_lshlrev_b32_e32 v211, 16, v117
	v_and_b32_e32 v207, 0xffff0000, v117
	v_lshlrev_b32_e32 v159, 16, v97
	v_and_b32_e32 v214, 0xffff0000, v93
	v_and_b32_e32 v215, 0xffff0000, v97
	v_and_b32_e32 v166, 0xffff0000, v91
	v_lshlrev_b32_e32 v210, 16, v113
	v_and_b32_e32 v206, 0xffff0000, v113
	v_lshlrev_b32_e32 v113, 16, v133
	v_and_b32_e32 v219, 0xffff0000, v133
	v_lshlrev_b32_e32 v221, 16, v132
	v_and_b32_e32 v227, 0xffff0000, v132
	v_and_b32_e32 v167, 0xffff0000, v95
	s_waitcnt vmcnt(20)
	v_lshlrev_b32_e32 v220, 16, v136
	v_and_b32_e32 v226, 0xffff0000, v136
	v_lshlrev_b32_e32 v192, 16, v112
	v_and_b32_e32 v204, 0xffff0000, v112
	v_lshlrev_b32_e32 v112, 16, v137
	v_and_b32_e32 v218, 0xffff0000, v137
	v_lshlrev_b32_e32 v231, 16, v130
	v_lshlrev_b32_e32 v230, 16, v134
	v_and_b32_e32 v134, 0xffff0000, v134
	v_pk_add_f32 v[196:197], v[220:221], v[226:227]
	v_lshlrev_b32_e32 v176, 16, v126
	v_and_b32_e32 v174, 0xffff0000, v126
	v_lshlrev_b32_e32 v177, 16, v122
	v_and_b32_e32 v175, 0xffff0000, v122
	v_lshlrev_b32_e32 v189, 16, v115
	v_and_b32_e32 v191, 0xffff0000, v115
	v_lshlrev_b32_e32 v239, 16, v114
	v_and_b32_e32 v241, 0xffff0000, v114
	v_pk_add_f32 v[114:115], v[112:113], v[218:219]
	v_lshlrev_b32_e32 v217, 16, v123
	v_lshlrev_b32_e32 v216, 16, v127
	v_and_b32_e32 v213, 0xffff0000, v123
	v_and_b32_e32 v212, 0xffff0000, v127
	v_pk_add_f32 v[126:127], v[216:217], v[212:213]
	v_lshlrev_b32_e32 v225, 16, v124
	v_lshlrev_b32_e32 v224, 16, v128
	v_and_b32_e32 v223, 0xffff0000, v124
	v_and_b32_e32 v222, 0xffff0000, v128
	v_pk_add_f32 v[234:235], v[224:225], v[222:223]
	v_lshlrev_b32_e32 v237, 16, v125
	v_lshlrev_b32_e32 v236, 16, v129
	v_and_b32_e32 v229, 0xffff0000, v125
	v_and_b32_e32 v228, 0xffff0000, v129
	v_pk_add_f32 v[124:125], v[236:237], v[228:229]
	v_lshlrev_b32_e32 v185, 16, v106
	v_lshlrev_b32_e32 v184, 16, v118
	v_and_b32_e32 v123, 0xffff0000, v106
	v_and_b32_e32 v122, 0xffff0000, v118
	v_pk_add_f32 v[128:129], v[184:185], v[122:123]
	v_lshlrev_b32_e32 v195, 16, v107
	v_lshlrev_b32_e32 v194, 16, v119
	v_and_b32_e32 v187, 0xffff0000, v107
	v_and_b32_e32 v186, 0xffff0000, v119
	v_pk_add_f32 v[106:107], v[194:195], v[186:187]
	v_lshlrev_b32_e32 v201, 16, v108
	v_lshlrev_b32_e32 v200, 16, v120
	v_and_b32_e32 v199, 0xffff0000, v108
	v_and_b32_e32 v198, 0xffff0000, v120
	v_pk_add_f32 v[118:119], v[200:201], v[198:199]
	v_lshlrev_b32_e32 v209, 16, v109
	v_lshlrev_b32_e32 v208, 16, v121
	v_and_b32_e32 v203, 0xffff0000, v109
	v_and_b32_e32 v202, 0xffff0000, v121
	v_pk_add_f32 v[108:109], v[208:209], v[202:203]
	v_lshlrev_b32_e32 v238, 16, v110
	v_and_b32_e32 v240, 0xffff0000, v110
	v_lshlrev_b32_e32 v188, 16, v111
	v_and_b32_e32 v190, 0xffff0000, v111
	v_pk_add_f32 v[110:111], v[238:239], v[240:241]
	v_pk_add_f32 v[178:179], v[188:189], v[190:191]
	v_lshlrev_b32_e32 v193, 16, v116
	v_and_b32_e32 v205, 0xffff0000, v116
	v_pk_add_f32 v[180:181], v[192:193], v[204:205]
	v_pk_add_f32 v[182:183], v[210:211], v[206:207]
	s_waitcnt lgkmcnt(2)
	v_mov_b32_e32 v116, v140
	s_waitcnt lgkmcnt(0)
	v_mov_b32_e32 v117, v100
	v_mul_f32_e32 v100, 0xbfb8aa3b, v158
	v_exp_f32_e32 v100, v100
	v_lshlrev_b32_e32 v140, 16, v89
	v_mov_b32_e32 v164, v144
	v_mov_b32_e32 v165, v104
	v_add_f32_e32 v100, 1.0, v100
	v_rcp_f32_e32 v160, v100
	v_mul_f32_e32 v100, 0xbfb8aa3b, v159
	v_exp_f32_e32 v100, v100
	v_mov_b32_e32 v104, v145
	s_cmpk_lt_i32 s6, 0x4400
	v_add_f32_e32 v100, 1.0, v100
	v_rcp_f32_e32 v161, v100
	v_mov_b32_e32 v100, v141
	v_lshlrev_b32_e32 v141, 16, v85
	v_pk_mul_f32 v[158:159], v[160:161], v[158:159]
	v_lshlrev_b32_e32 v160, 16, v92
	v_mul_f32_e32 v93, 0xbfb8aa3b, v160
	v_exp_f32_e32 v93, v93
	v_lshlrev_b32_e32 v161, 16, v96
	v_and_b32_e32 v92, 0xffff0000, v92
	v_add_f32_e32 v93, 1.0, v93
	v_rcp_f32_e32 v162, v93
	v_mul_f32_e32 v93, 0xbfb8aa3b, v161
	v_exp_f32_e32 v93, v93
	s_nop 0
	v_add_f32_e32 v93, 1.0, v93
	v_rcp_f32_e32 v163, v93
	v_and_b32_e32 v93, 0xffff0000, v96
	v_mul_f32_e32 v96, 0xbfb8aa3b, v92
	v_mul_f32_e32 v97, 0xbfb8aa3b, v93
	v_exp_f32_e32 v96, v96
	v_exp_f32_e32 v97, v97
	v_pk_mul_f32 v[160:161], v[162:163], v[160:161]
	v_mov_b32_e32 v163, v98
	v_add_f32_e32 v96, 1.0, v96
	v_add_f32_e32 v97, 1.0, v97
	v_rcp_f32_e32 v96, v96
	v_rcp_f32_e32 v97, v97
	v_mov_b32_e32 v162, v138
	v_pk_mul_f32 v[132:133], v[96:97], v[92:93]
	v_lshlrev_b32_e32 v96, 16, v91
	v_mul_f32_e32 v91, 0xbfb8aa3b, v166
	v_exp_f32_e32 v91, v91
	v_mul_f32_e32 v98, 0xbfb8aa3b, v96
	v_exp_f32_e32 v98, v98
	v_lshlrev_b32_e32 v97, 16, v95
	v_add_f32_e32 v91, 1.0, v91
	v_rcp_f32_e32 v168, v91
	v_mul_f32_e32 v91, 0xbfb8aa3b, v167
	v_exp_f32_e32 v91, v91
	v_add_f32_e32 v98, 1.0, v98
	v_rcp_f32_e32 v136, v98
	v_mul_f32_e32 v98, 0xbfb8aa3b, v97
	v_add_f32_e32 v91, 1.0, v91
	v_rcp_f32_e32 v169, v91
	v_exp_f32_e32 v98, v98
	v_lshlrev_b32_e32 v92, 16, v135
	v_lshlrev_b32_e32 v93, 16, v131
	v_pk_mul_f32 v[166:167], v[168:169], v[166:167]
	v_lshlrev_b32_e32 v168, 16, v90
	v_mul_f32_e32 v91, 0xbfb8aa3b, v168
	v_exp_f32_e32 v91, v91
	v_lshlrev_b32_e32 v169, 16, v94
	v_and_b32_e32 v90, 0xffff0000, v90
	v_add_f32_e32 v98, 1.0, v98
	v_add_f32_e32 v91, 1.0, v91
	v_rcp_f32_e32 v172, v91
	v_mul_f32_e32 v91, 0xbfb8aa3b, v169
	v_exp_f32_e32 v91, v91
	v_rcp_f32_e32 v137, v98
	v_mov_b32_e32 v98, v139
	v_add_f32_e32 v91, 1.0, v91
	v_rcp_f32_e32 v173, v91
	v_and_b32_e32 v91, 0xffff0000, v94
	v_mul_f32_e32 v94, 0xbfb8aa3b, v90
	v_mul_f32_e32 v95, 0xbfb8aa3b, v91
	v_exp_f32_e32 v94, v94
	v_exp_f32_e32 v95, v95
	v_pk_mul_f32 v[136:137], v[136:137], v[96:97]
	v_and_b32_e32 v96, 0xffff0000, v135
	v_add_f32_e32 v94, 1.0, v94
	v_add_f32_e32 v95, 1.0, v95
	v_rcp_f32_e32 v94, v94
	v_rcp_f32_e32 v95, v95
	v_and_b32_e32 v135, 0xffff0000, v130
	v_and_b32_e32 v97, 0xffff0000, v131
	v_pk_mul_f32 v[168:169], v[172:173], v[168:169]
	v_pk_mul_f32 v[130:131], v[94:95], v[90:91]
	v_pk_add_f32 v[94:95], v[230:231], v[134:135]
	v_pk_add_f32 v[90:91], v[92:93], v[96:97]
	v_pk_add_f32 v[94:95], v[94:95], 0 op_sel_hi:[1,0]
	v_mov_b32_e32 v172, v142
	v_pk_add_f32 v[90:91], v[90:91], v[94:95]
	v_pk_add_f32 v[94:95], v[176:177], v[174:175]
	v_pk_add_f32 v[90:91], v[196:197], v[90:91]
	v_mov_b32_e32 v173, v102
	v_pk_add_f32 v[90:91], v[114:115], v[90:91]
	v_mov_b32_e32 v102, v143
	v_pk_add_f32 v[90:91], v[94:95], v[90:91]
	v_mov_b32_e32 v94, 0
	v_pk_add_f32 v[90:91], v[126:127], v[90:91]
	v_mov_b32_e32 v95, 0
	v_pk_add_f32 v[90:91], v[234:235], v[90:91]
	v_mul_f32_e32 v142, 0xbfb8aa3b, v140
	v_pk_add_f32 v[90:91], v[124:125], v[90:91]
	v_mul_f32_e32 v143, 0xbfb8aa3b, v141
	v_pk_add_f32 v[90:91], v[128:129], v[90:91]
	v_exp_f32_e32 v142, v142
	v_pk_add_f32 v[90:91], v[106:107], v[90:91]
	v_exp_f32_e32 v143, v143
	v_pk_add_f32 v[90:91], v[118:119], v[90:91]
	v_add_f32_e32 v142, 1.0, v142
	v_pk_add_f32 v[90:91], v[108:109], v[90:91]
	v_add_f32_e32 v143, 1.0, v143
	v_pk_add_f32 v[90:91], v[110:111], v[90:91]
	v_rcp_f32_e32 v142, v142
	v_pk_add_f32 v[90:91], v[178:179], v[90:91]
	v_rcp_f32_e32 v143, v143
	v_pk_add_f32 v[90:91], v[180:181], v[90:91]
	v_pk_mul_f32 v[140:141], v[142:143], v[140:141]
	v_pk_add_f32 v[90:91], v[182:183], v[90:91]
	s_nop 1
	v_mov_b32_dpp v94, v90 row_ror:8 row_mask:0xf bank_mask:0xf
	v_mov_b32_dpp v95, v91 row_ror:8 row_mask:0xf bank_mask:0xf
	v_pk_add_f32 v[90:91], v[90:91], v[94:95]
	v_mov_b32_e32 v94, 0
	v_mov_b32_e32 v95, 0
	s_nop 0
	v_mov_b32_dpp v94, v90 row_ror:4 row_mask:0xf bank_mask:0xf
	v_mov_b32_dpp v95, v91 row_ror:4 row_mask:0xf bank_mask:0xf
	v_pk_add_f32 v[90:91], v[90:91], v[94:95]
	v_mov_b32_e32 v94, 0
	v_mov_b32_e32 v95, 0
	s_nop 0
	v_mov_b32_dpp v94, v90 row_ror:2 row_mask:0xf bank_mask:0xf
	v_mov_b32_dpp v95, v91 row_ror:2 row_mask:0xf bank_mask:0xf
	v_pk_add_f32 v[90:91], v[90:91], v[94:95]
	v_mov_b32_e32 v94, 0
	v_mov_b32_e32 v95, 0
	s_nop 0
	v_mov_b32_dpp v94, v90 row_ror:1 row_mask:0xf bank_mask:0xf
	v_mov_b32_dpp v95, v91 row_ror:1 row_mask:0xf bank_mask:0xf
	v_pk_add_f32 v[196:197], v[90:91], v[94:95]
	s_nop 0
	v_pk_fma_f32 v[180:181], v[196:197], s[14:15], v[134:135] op_sel_hi:[1,0,1] neg_lo:[1,0,0] neg_hi:[1,0,0]
	v_pk_fma_f32 v[134:135], v[196:197], s[14:15], v[96:97] op_sel_hi:[1,0,1] neg_lo:[1,0,0] neg_hi:[1,0,0]
	v_pk_fma_f32 v[182:183], v[196:197], s[14:15], v[230:231] op_sel_hi:[1,0,1] neg_lo:[1,0,0] neg_hi:[1,0,0]
	v_pk_mul_f32 v[90:91], v[180:181], v[180:181]
	v_pk_fma_f32 v[178:179], v[196:197], s[14:15], v[92:93] op_sel_hi:[1,0,1] neg_lo:[1,0,0] neg_hi:[1,0,0]
	v_pk_mul_f32 v[92:93], v[134:135], v[134:135]
	v_pk_fma_f32 v[90:91], v[182:183], v[182:183], v[90:91]
	v_pk_fma_f32 v[92:93], v[178:179], v[178:179], v[92:93]
	v_pk_fma_f32 v[126:127], v[196:197], s[14:15], v[226:227] op_sel_hi:[1,0,1] neg_lo:[1,0,0] neg_hi:[1,0,0]
	v_pk_add_f32 v[90:91], v[90:91], v[92:93]
	v_pk_fma_f32 v[128:129], v[196:197], s[14:15], v[220:221] op_sel_hi:[1,0,1] neg_lo:[1,0,0] neg_hi:[1,0,0]
	v_pk_mul_f32 v[92:93], v[126:127], v[126:127]
	v_pk_fma_f32 v[120:121], v[196:197], s[14:15], v[218:219] op_sel_hi:[1,0,1] neg_lo:[1,0,0] neg_hi:[1,0,0]
	v_pk_fma_f32 v[92:93], v[128:129], v[128:129], v[92:93]
	v_pk_fma_f32 v[124:125], v[196:197], s[14:15], v[112:113] op_sel_hi:[1,0,1] neg_lo:[1,0,0] neg_hi:[1,0,0]
	v_pk_add_f32 v[90:91], v[92:93], v[90:91]
	v_pk_mul_f32 v[92:93], v[120:121], v[120:121]
	v_pk_mul_f32 v[118:119], v[196:197], s[14:15] op_sel_hi:[1,0]
	v_pk_fma_f32 v[92:93], v[124:125], v[124:125], v[92:93]
	v_and_b32_e32 v227, 0xffff0000, v85
	v_pk_add_f32 v[218:219], v[92:93], v[90:91]
	v_mov_b32_e32 v90, v188
	v_mov_b32_e32 v91, v238
	v_pk_add_f32 v[110:111], v[90:91], v[118:119] op_sel_hi:[1,0] neg_lo:[0,1] neg_hi:[0,1]
	v_mov_b32_e32 v90, v190
	v_mov_b32_e32 v91, v240
	v_pk_add_f32 v[106:107], v[90:91], v[118:119] op_sel_hi:[1,0] neg_lo:[0,1] neg_hi:[0,1]
	v_mov_b32_e32 v240, v191
	v_pk_mul_f32 v[90:91], v[106:107], v[106:107]
	v_mov_b32_e32 v238, v189
	v_pk_add_f32 v[108:109], v[240:241], v[118:119] op_sel:[0,1] neg_lo:[0,1] neg_hi:[0,1]
	v_pk_fma_f32 v[114:115], v[110:111], v[110:111], v[90:91]
	v_pk_add_f32 v[112:113], v[238:239], v[118:119] op_sel:[0,1] neg_lo:[0,1] neg_hi:[0,1]
	v_pk_mul_f32 v[90:91], v[108:109], v[108:109]
	v_pk_fma_f32 v[142:143], v[196:197], s[14:15], v[228:229] op_sel_hi:[1,0,1] neg_lo:[1,0,0] neg_hi:[1,0,0]
	v_pk_fma_f32 v[188:189], v[112:113], v[112:113], v[90:91]
	v_mov_b32_e32 v90, v210
	v_mov_b32_e32 v91, v192
	v_pk_add_f32 v[94:95], v[90:91], v[118:119] op_sel_hi:[1,0] neg_lo:[0,1] neg_hi:[0,1]
	v_mov_b32_e32 v90, v206
	v_mov_b32_e32 v91, v204
	v_pk_add_f32 v[90:91], v[90:91], v[118:119] op_sel_hi:[1,0] neg_lo:[0,1] neg_hi:[0,1]
	v_mov_b32_e32 v204, v207
	v_pk_mul_f32 v[92:93], v[90:91], v[90:91]
	v_mov_b32_e32 v192, v211
	v_pk_fma_f32 v[190:191], v[94:95], v[94:95], v[92:93]
	v_pk_add_f32 v[92:93], v[204:205], v[118:119] op_sel:[0,1] neg_lo:[0,1] neg_hi:[0,1]
	v_lshlrev_b32_e32 v204, 16, v88
	v_mul_f32_e32 v85, 0xbfb8aa3b, v204
	v_exp_f32_e32 v85, v85
	v_pk_add_f32 v[96:97], v[192:193], v[118:119] op_sel:[0,1] neg_lo:[0,1] neg_hi:[0,1]
	v_pk_mul_f32 v[118:119], v[92:93], v[92:93]
	v_lshlrev_b32_e32 v205, 16, v84
	v_add_f32_e32 v85, 1.0, v85
	v_pk_fma_f32 v[192:193], v[96:97], v[96:97], v[118:119]
	v_mul_f32_e32 v118, 0xbfb8aa3b, v214
	v_mul_f32_e32 v119, 0xbfb8aa3b, v215
	v_rcp_f32_e32 v206, v85
	v_mul_f32_e32 v85, 0xbfb8aa3b, v205
	v_exp_f32_e32 v118, v118
	v_exp_f32_e32 v119, v119
	v_exp_f32_e32 v85, v85
	v_pk_mul_f32 v[144:145], v[142:143], v[142:143]
	v_add_f32_e32 v118, 1.0, v118
	v_add_f32_e32 v119, 1.0, v119
	v_add_f32_e32 v85, 1.0, v85
	v_rcp_f32_e32 v118, v118
	v_rcp_f32_e32 v119, v119
	v_rcp_f32_e32 v207, v85
	v_and_b32_e32 v85, 0xffff0000, v84
	v_and_b32_e32 v84, 0xffff0000, v88
	v_pk_mul_f32 v[138:139], v[118:119], v[214:215]
	v_pk_fma_f32 v[118:119], v[196:197], s[14:15], v[236:237] op_sel_hi:[1,0,1] neg_lo:[1,0,0] neg_hi:[1,0,0]
	v_pk_mul_f32 v[204:205], v[206:207], v[204:205]
	v_pk_fma_f32 v[206:207], v[196:197], s[14:15], v[222:223] op_sel_hi:[1,0,1] neg_lo:[1,0,0] neg_hi:[1,0,0]
	v_pk_fma_f32 v[228:229], v[118:119], v[118:119], v[144:145]
	v_pk_fma_f32 v[144:145], v[196:197], s[14:15], v[224:225] op_sel_hi:[1,0,1] neg_lo:[1,0,0] neg_hi:[1,0,0]
	v_pk_mul_f32 v[210:211], v[206:207], v[206:207]
	v_and_b32_e32 v226, 0xffff0000, v89
	v_pk_fma_f32 v[222:223], v[144:145], v[144:145], v[210:211]
	v_lshlrev_b32_e32 v211, 16, v83
	v_lshlrev_b32_e32 v210, 16, v87
	v_mul_f32_e32 v214, 0xbfb8aa3b, v210
	v_mul_f32_e32 v215, 0xbfb8aa3b, v211
	v_exp_f32_e32 v214, v214
	v_exp_f32_e32 v215, v215
	v_mul_f32_e32 v88, 0xbfb8aa3b, v84
	v_mul_f32_e32 v89, 0xbfb8aa3b, v85
	v_add_f32_e32 v214, 1.0, v214
	v_add_f32_e32 v215, 1.0, v215
	v_rcp_f32_e32 v214, v214
	v_rcp_f32_e32 v215, v215
	v_exp_f32_e32 v88, v88
	v_exp_f32_e32 v89, v89
	v_pk_fma_f32 v[212:213], v[196:197], s[14:15], v[212:213] op_sel_hi:[1,0,1] neg_lo:[1,0,0] neg_hi:[1,0,0]
	v_pk_mul_f32 v[210:211], v[214:215], v[210:211]
	v_and_b32_e32 v214, 0xffff0000, v87
	v_and_b32_e32 v215, 0xffff0000, v83
	v_mul_f32_e32 v83, 0xbfb8aa3b, v214
	v_exp_f32_e32 v83, v83
	v_add_f32_e32 v88, 1.0, v88
	v_add_f32_e32 v89, 1.0, v89
	v_rcp_f32_e32 v88, v88
	v_add_f32_e32 v83, 1.0, v83
	v_rcp_f32_e32 v89, v89
	v_rcp_f32_e32 v220, v83
	v_mul_f32_e32 v83, 0xbfb8aa3b, v215
	v_exp_f32_e32 v83, v83
	v_pk_mul_f32 v[84:85], v[88:89], v[84:85]
	v_pk_fma_f32 v[88:89], v[196:197], s[14:15], v[216:217] op_sel_hi:[1,0,1] neg_lo:[1,0,0] neg_hi:[1,0,0]
	v_pk_mul_f32 v[216:217], v[212:213], v[212:213]
	v_add_f32_e32 v83, 1.0, v83
	v_pk_fma_f32 v[224:225], v[88:89], v[88:89], v[216:217]
	v_lshlrev_b32_e32 v216, 16, v86
	v_rcp_f32_e32 v221, v83
	v_mul_f32_e32 v83, 0xbfb8aa3b, v216
	v_exp_f32_e32 v83, v83
	v_lshlrev_b32_e32 v217, 16, v82
	v_pk_mul_f32 v[214:215], v[220:221], v[214:215]
	v_pk_fma_f32 v[174:175], v[196:197], s[14:15], v[174:175] op_sel_hi:[1,0,1] neg_lo:[1,0,0] neg_hi:[1,0,0]
	v_add_f32_e32 v83, 1.0, v83
	v_rcp_f32_e32 v220, v83
	v_mul_f32_e32 v83, 0xbfb8aa3b, v217
	v_exp_f32_e32 v83, v83
	v_pk_fma_f32 v[176:177], v[196:197], s[14:15], v[176:177] op_sel_hi:[1,0,1] neg_lo:[1,0,0] neg_hi:[1,0,0]
	v_pk_mul_f32 v[230:231], v[174:175], v[174:175]
	v_pk_fma_f32 v[202:203], v[196:197], s[14:15], v[202:203] op_sel_hi:[1,0,1] neg_lo:[1,0,0] neg_hi:[1,0,0]
	v_add_f32_e32 v83, 1.0, v83
	v_rcp_f32_e32 v221, v83
	v_and_b32_e32 v83, 0xffff0000, v82
	v_and_b32_e32 v82, 0xffff0000, v86
	v_mul_f32_e32 v86, 0xbfb8aa3b, v82
	v_mul_f32_e32 v87, 0xbfb8aa3b, v83
	v_exp_f32_e32 v86, v86
	v_exp_f32_e32 v87, v87
	v_pk_mul_f32 v[216:217], v[220:221], v[216:217]
	v_pk_fma_f32 v[198:199], v[196:197], s[14:15], v[198:199] op_sel_hi:[1,0,1] neg_lo:[1,0,0] neg_hi:[1,0,0]
	v_add_f32_e32 v86, 1.0, v86
	v_add_f32_e32 v87, 1.0, v87
	v_rcp_f32_e32 v86, v86
	v_rcp_f32_e32 v87, v87
	v_pk_fma_f32 v[200:201], v[196:197], s[14:15], v[200:201] op_sel_hi:[1,0,1] neg_lo:[1,0,0] neg_hi:[1,0,0]
	v_pk_fma_f32 v[186:187], v[196:197], s[14:15], v[186:187] op_sel_hi:[1,0,1] neg_lo:[1,0,0] neg_hi:[1,0,0]
	v_pk_fma_f32 v[184:185], v[196:197], s[14:15], v[184:185] op_sel_hi:[1,0,1] neg_lo:[1,0,0] neg_hi:[1,0,0]
	v_pk_mul_f32 v[220:221], v[86:87], v[82:83]
	v_pk_fma_f32 v[82:83], v[176:177], v[176:177], v[230:231]
	v_pk_mul_f32 v[234:235], v[186:187], v[186:187]
	v_pk_add_f32 v[82:83], v[82:83], v[218:219]
	s_nop 0
	v_pk_add_f32 v[82:83], v[224:225], v[82:83]
	s_nop 0
	v_pk_add_f32 v[82:83], v[222:223], v[82:83]
	v_pk_mul_f32 v[222:223], v[202:203], v[202:203]
	v_pk_add_f32 v[224:225], v[228:229], v[82:83]
	v_mul_f32_e32 v82, 0xbfb8aa3b, v226
	v_mul_f32_e32 v83, 0xbfb8aa3b, v227
	v_exp_f32_e32 v82, v82
	v_exp_f32_e32 v83, v83
	v_add_f32_e32 v82, 1.0, v82
	v_add_f32_e32 v83, 1.0, v83
	v_rcp_f32_e32 v82, v82
	v_rcp_f32_e32 v83, v83
	s_nop 0
	v_pk_mul_f32 v[86:87], v[82:83], v[226:227]
	v_pk_fma_f32 v[82:83], v[196:197], s[14:15], v[208:209] op_sel_hi:[1,0,1] neg_lo:[1,0,0] neg_hi:[1,0,0]
	v_lshlrev_b32_e32 v209, 16, v81
	v_lshlrev_b32_e32 v208, 16, v77
	v_mul_f32_e32 v218, 0xbfb8aa3b, v208
	v_mul_f32_e32 v219, 0xbfb8aa3b, v209
	v_exp_f32_e32 v218, v218
	v_exp_f32_e32 v219, v219
	v_pk_fma_f32 v[228:229], v[82:83], v[82:83], v[222:223]
	v_lshlrev_b32_e32 v222, 16, v76
	v_add_f32_e32 v218, 1.0, v218
	v_add_f32_e32 v219, 1.0, v219
	v_rcp_f32_e32 v218, v218
	v_rcp_f32_e32 v219, v219
	v_lshlrev_b32_e32 v223, 16, v80
	v_and_b32_e32 v76, 0xffff0000, v76
	v_pk_mul_f32 v[208:209], v[218:219], v[208:209]
	v_and_b32_e32 v218, 0xffff0000, v77
	v_mul_f32_e32 v77, 0xbfb8aa3b, v222
	v_exp_f32_e32 v77, v77
	v_and_b32_e32 v219, 0xffff0000, v81
	v_add_f32_e32 v77, 1.0, v77
	v_rcp_f32_e32 v226, v77
	v_mul_f32_e32 v77, 0xbfb8aa3b, v223
	v_exp_f32_e32 v77, v77
	s_nop 0
	v_add_f32_e32 v77, 1.0, v77
	v_rcp_f32_e32 v227, v77
	v_and_b32_e32 v77, 0xffff0000, v80
	v_mul_f32_e32 v80, 0xbfb8aa3b, v76
	v_mul_f32_e32 v81, 0xbfb8aa3b, v77
	v_exp_f32_e32 v80, v80
	v_exp_f32_e32 v81, v81
	v_pk_mul_f32 v[222:223], v[226:227], v[222:223]
	v_pk_mul_f32 v[226:227], v[198:199], v[198:199]
	v_add_f32_e32 v80, 1.0, v80
	v_add_f32_e32 v81, 1.0, v81
	v_rcp_f32_e32 v80, v80
	v_rcp_f32_e32 v81, v81
	v_pk_fma_f32 v[230:231], v[200:201], v[200:201], v[226:227]
	v_pk_mul_f32 v[76:77], v[80:81], v[76:77]
	v_pk_fma_f32 v[80:81], v[196:197], s[14:15], v[194:195] op_sel_hi:[1,0,1] neg_lo:[1,0,0] neg_hi:[1,0,0]
	v_lshlrev_b32_e32 v195, 16, v79
	v_lshlrev_b32_e32 v194, 16, v75
	v_mul_f32_e32 v226, 0xbfb8aa3b, v194
	v_mul_f32_e32 v227, 0xbfb8aa3b, v195
	v_exp_f32_e32 v226, v226
	v_exp_f32_e32 v227, v227
	v_pk_fma_f32 v[196:197], v[196:197], s[14:15], v[122:123] op_sel_hi:[1,0,1] neg_lo:[1,0,0] neg_hi:[1,0,0]
	v_pk_fma_f32 v[234:235], v[80:81], v[80:81], v[234:235]
	v_add_f32_e32 v226, 1.0, v226
	v_add_f32_e32 v227, 1.0, v227
	v_rcp_f32_e32 v226, v226
	v_rcp_f32_e32 v227, v227
	v_pk_mul_f32 v[122:123], v[196:197], v[196:197]
	v_pk_mul_f32 v[194:195], v[226:227], v[194:195]
	v_and_b32_e32 v226, 0xffff0000, v75
	v_mul_f32_e32 v75, 0xbfb8aa3b, v226
	v_exp_f32_e32 v75, v75
	v_and_b32_e32 v227, 0xffff0000, v79
	v_add_f32_e32 v75, 1.0, v75
	v_rcp_f32_e32 v236, v75
	v_mul_f32_e32 v75, 0xbfb8aa3b, v227
	v_exp_f32_e32 v75, v75
	s_nop 0
	v_add_f32_e32 v75, 1.0, v75
	v_rcp_f32_e32 v237, v75
	s_nop 0
	v_pk_mul_f32 v[226:227], v[236:237], v[226:227]
	v_lshlrev_b32_e32 v236, 16, v74
	v_mul_f32_e32 v75, 0xbfb8aa3b, v236
	v_exp_f32_e32 v75, v75
	v_lshlrev_b32_e32 v237, 16, v78
	v_and_b32_e32 v74, 0xffff0000, v74
	v_add_f32_e32 v75, 1.0, v75
	v_rcp_f32_e32 v238, v75
	v_mul_f32_e32 v75, 0xbfb8aa3b, v237
	v_exp_f32_e32 v75, v75
	s_nop 0
	v_add_f32_e32 v75, 1.0, v75
	v_rcp_f32_e32 v239, v75
	v_and_b32_e32 v75, 0xffff0000, v78
	v_mul_f32_e32 v78, 0xbfb8aa3b, v74
	v_mul_f32_e32 v79, 0xbfb8aa3b, v75
	v_exp_f32_e32 v78, v78
	v_exp_f32_e32 v79, v79
	v_pk_mul_f32 v[236:237], v[238:239], v[236:237]
	v_add_f32_e32 v78, 1.0, v78
	v_add_f32_e32 v79, 1.0, v79
	v_rcp_f32_e32 v78, v78
	v_rcp_f32_e32 v79, v79
	s_nop 0
	v_pk_mul_f32 v[74:75], v[78:79], v[74:75]
	v_pk_fma_f32 v[78:79], v[184:185], v[184:185], v[122:123]
	s_nop 0
	v_pk_add_f32 v[78:79], v[78:79], v[224:225]
	s_nop 0
	v_pk_add_f32 v[78:79], v[234:235], v[78:79]
	s_nop 0
	v_pk_add_f32 v[78:79], v[230:231], v[78:79]
	s_nop 0
	v_pk_add_f32 v[78:79], v[228:229], v[78:79]
	s_nop 0
	v_add_f32_e32 v78, v115, v78
	v_add_f32_e32 v78, v114, v78
	v_add_f32_e32 v78, v191, v78
	v_add_f32_e32 v78, v190, v78
	v_add_f32_e32 v79, v189, v79
	v_add_f32_e32 v79, v188, v79
	v_add_f32_dpp v78, v78, v78 row_ror:8 row_mask:0xf bank_mask:0xf bound_ctrl:1
	v_add_f32_e32 v79, v193, v79
	v_add_f32_e32 v79, v192, v79
	v_add_f32_dpp v78, v78, v78 row_ror:4 row_mask:0xf bank_mask:0xf bound_ctrl:1
	s_nop 0
	v_add_f32_dpp v79, v79, v79 row_ror:8 row_mask:0xf bank_mask:0xf bound_ctrl:1
	v_add_f32_dpp v78, v78, v78 row_ror:2 row_mask:0xf bank_mask:0xf bound_ctrl:1
	s_nop 0
	v_add_f32_dpp v79, v79, v79 row_ror:4 row_mask:0xf bank_mask:0xf bound_ctrl:1
	v_add_f32_dpp v78, v78, v78 row_ror:1 row_mask:0xf bank_mask:0xf bound_ctrl:1
	v_fmamk_f32 v78, v78, 0x3b000000, v1
	v_cmp_gt_f32_e32 vcc, s9, v78
	v_mul_f32_e32 v114, 0x4f800000, v78
	v_add_f32_dpp v79, v79, v79 row_ror:2 row_mask:0xf bank_mask:0xf bound_ctrl:1
	v_cndmask_b32_e32 v78, v78, v114, vcc
	v_sqrt_f32_e32 v114, v78
	v_add_f32_dpp v79, v79, v79 row_ror:1 row_mask:0xf bank_mask:0xf bound_ctrl:1
	v_fmamk_f32 v79, v79, 0x3b000000, v1
	v_add_u32_e32 v115, -1, v114
	v_fma_f32 v122, -v115, v114, v78
	v_cmp_ge_f32_e64 s[4:5], 0, v122
	v_add_u32_e32 v122, 1, v114
	s_nop 0
	v_cndmask_b32_e64 v115, v114, v115, s[4:5]
	v_fma_f32 v114, -v122, v114, v78
	v_cmp_lt_f32_e64 s[4:5], 0, v114
	s_nop 1
	v_cndmask_b32_e64 v114, v115, v122, s[4:5]
	v_mul_f32_e32 v115, 0x37800000, v114
	v_cndmask_b32_e32 v114, v114, v115, vcc
	v_cmp_class_f32_e32 vcc, v78, v171
	s_nop 1
	v_cndmask_b32_e32 v78, v114, v78, vcc
	v_cmp_gt_f32_e32 vcc, s9, v79
	v_mul_f32_e32 v114, 0x4f800000, v79
	s_nop 0
	v_cndmask_b32_e32 v79, v79, v114, vcc
	v_sqrt_f32_e32 v114, v79
	s_nop 0
	v_add_u32_e32 v115, -1, v114
	v_fma_f32 v122, -v115, v114, v79
	v_cmp_ge_f32_e64 s[4:5], 0, v122
	v_add_u32_e32 v122, 1, v114
	s_nop 0
	v_cndmask_b32_e64 v115, v114, v115, s[4:5]
	v_fma_f32 v114, -v122, v114, v79
	v_cmp_lt_f32_e64 s[4:5], 0, v114
	s_nop 1
	v_cndmask_b32_e64 v114, v115, v122, s[4:5]
	v_mul_f32_e32 v115, 0x37800000, v114
	v_cndmask_b32_e32 v114, v114, v115, vcc
	v_cmp_class_f32_e32 vcc, v79, v171
	s_nop 1
	v_cndmask_b32_e32 v79, v114, v79, vcc
	v_div_scale_f32 v114, s[4:5], v79, v79, 1.0
	v_rcp_f32_e32 v115, v114
	s_nop 0
	v_fma_f32 v122, -v114, v115, 1.0
	v_fmac_f32_e32 v115, v122, v115
	v_div_scale_f32 v122, vcc, 1.0, v79, 1.0
	v_mul_f32_e32 v123, v122, v115
	v_fma_f32 v188, -v114, v123, v122
	v_fmac_f32_e32 v123, v188, v115
	v_fma_f32 v114, -v114, v123, v122
	v_div_fmas_f32 v114, v114, v115, v123
	v_div_fixup_f32 v115, v114, v79, 1.0
	v_div_scale_f32 v79, s[4:5], v78, v78, 1.0
	v_rcp_f32_e32 v114, v79
	s_nop 0
	v_fma_f32 v122, -v79, v114, 1.0
	v_fmac_f32_e32 v114, v122, v114
	v_div_scale_f32 v122, vcc, 1.0, v78, 1.0
	v_mul_f32_e32 v123, v122, v114
	v_fma_f32 v188, -v79, v123, v122
	v_fmac_f32_e32 v123, v188, v114
	v_fma_f32 v79, -v79, v123, v122
	v_div_fmas_f32 v79, v79, v114, v123
	v_div_fixup_f32 v114, v79, v78, 1.0
	v_pk_mul_f32 v[78:79], v[182:183], v[114:115]
	v_pk_mul_f32 v[122:123], v[180:181], v[114:115]
	v_pk_mul_f32 v[78:79], v[172:173], v[78:79]
	v_pk_mul_f32 v[102:103], v[102:103], v[122:123]
	v_pk_mul_f32 v[78:79], v[168:169], v[78:79]
	s_nop 0
	v_add_f32_e32 v122, v78, v79
	v_pk_mul_f32 v[78:79], v[130:131], v[102:103]
	s_nop 0
	v_add_f32_e32 v78, v78, v79
	v_cvt_pk_bf16_f32 v102, v122, v78
	v_pk_mul_f32 v[78:79], v[178:179], v[114:115]
	v_pk_mul_f32 v[122:123], v[134:135], v[114:115]
	v_pk_mul_f32 v[78:79], v[164:165], v[78:79]
	v_pk_mul_f32 v[104:105], v[104:105], v[122:123]
	v_pk_mul_f32 v[78:79], v[136:137], v[78:79]
	s_waitcnt vmcnt(15)
	v_mov_b64_e32 v[136:137], v[4:5]
	v_add_f32_e32 v103, v78, v79
	v_pk_mul_f32 v[78:79], v[166:167], v[104:105]
	v_pk_mul_f32 v[104:105], v[126:127], v[114:115]
	v_add_f32_e32 v78, v78, v79
	v_cvt_pk_bf16_f32 v103, v103, v78
	v_pk_mul_f32 v[78:79], v[128:129], v[114:115]
	v_pk_mul_f32 v[98:99], v[98:99], v[104:105]
	v_pk_mul_f32 v[78:79], v[162:163], v[78:79]
	v_mov_b64_e32 v[134:135], v[2:3]
	v_pk_mul_f32 v[78:79], v[160:161], v[78:79]
	s_nop 0
	v_add_f32_e32 v104, v78, v79
	v_pk_mul_f32 v[78:79], v[132:133], v[98:99]
	v_pk_mul_f32 v[98:99], v[120:121], v[114:115]
	v_add_f32_e32 v78, v78, v79
	v_cvt_pk_bf16_f32 v104, v104, v78
	v_pk_mul_f32 v[78:79], v[124:125], v[114:115]
	v_pk_mul_f32 v[98:99], v[100:101], v[98:99]
	v_pk_mul_f32 v[78:79], v[116:117], v[78:79]
	s_waitcnt vmcnt(14)
	v_mov_b64_e32 v[132:133], v[8:9]
	v_pk_mul_f32 v[78:79], v[158:159], v[78:79]
	v_mov_b64_e32 v[130:131], v[6:7]
	v_add_f32_e32 v100, v78, v79
	v_pk_mul_f32 v[78:79], v[138:139], v[98:99]
	s_nop 0
	v_add_f32_e32 v78, v78, v79
	v_cvt_pk_bf16_f32 v105, v100, v78
	global_store_dwordx4 v[156:157], v[102:105], off
	ds_read_b128 v[98:101], v242 offset:3072
	s_nop 0
	ds_read_b128 v[102:105], v242 offset:2048
	ds_read_b128 v[120:123], v242 offset:11264
	ds_read_b128 v[124:127], v242 offset:10240
	v_pk_mul_f32 v[78:79], v[176:177], v[114:115]
	s_waitcnt lgkmcnt(2)
	v_mov_b32_e32 v116, v102
	s_waitcnt lgkmcnt(0)
	v_mov_b32_e32 v117, v124
	v_pk_mul_f32 v[78:79], v[116:117], v[78:79]
	v_pk_mul_f32 v[116:117], v[174:175], v[114:115]
	v_mov_b32_e32 v124, v103
	v_pk_mul_f32 v[102:103], v[124:125], v[116:117]
	v_pk_mul_f32 v[78:79], v[216:217], v[78:79]
	s_nop 0
	v_add_f32_e32 v116, v78, v79
	v_pk_mul_f32 v[78:79], v[220:221], v[102:103]
	s_nop 0
	v_add_f32_e32 v78, v78, v79
	v_cvt_pk_bf16_f32 v102, v116, v78
	v_pk_mul_f32 v[78:79], v[88:89], v[114:115]
	v_mov_b32_e32 v88, v104
	v_mov_b32_e32 v89, v126
	v_pk_mul_f32 v[78:79], v[88:89], v[78:79]
	v_pk_mul_f32 v[88:89], v[212:213], v[114:115]
	v_mov_b32_e32 v126, v105
	v_pk_mul_f32 v[88:89], v[126:127], v[88:89]
	v_pk_mul_f32 v[78:79], v[210:211], v[78:79]
	s_waitcnt vmcnt(12)
	v_mov_b64_e32 v[128:129], v[12:13]
	v_add_f32_e32 v103, v78, v79
	v_pk_mul_f32 v[78:79], v[214:215], v[88:89]
	v_mov_b32_e32 v88, v98
	v_add_f32_e32 v78, v78, v79
	v_cvt_pk_bf16_f32 v103, v103, v78
	v_pk_mul_f32 v[78:79], v[144:145], v[114:115]
	v_mov_b32_e32 v89, v120
	v_pk_mul_f32 v[78:79], v[88:89], v[78:79]
	v_pk_mul_f32 v[88:89], v[206:207], v[114:115]
	v_mov_b32_e32 v120, v99
	v_pk_mul_f32 v[88:89], v[120:121], v[88:89]
	v_pk_mul_f32 v[78:79], v[204:205], v[78:79]
	v_mov_b64_e32 v[126:127], v[10:11]
	v_add_f32_e32 v98, v78, v79
	v_pk_mul_f32 v[78:79], v[84:85], v[88:89]
	v_mov_b32_e32 v84, v100
	v_add_f32_e32 v78, v78, v79
	v_cvt_pk_bf16_f32 v104, v98, v78
	v_pk_mul_f32 v[78:79], v[118:119], v[114:115]
	v_mov_b32_e32 v85, v122
	v_pk_mul_f32 v[78:79], v[84:85], v[78:79]
	v_pk_mul_f32 v[84:85], v[142:143], v[114:115]
	v_mov_b32_e32 v122, v101
	v_pk_mul_f32 v[84:85], v[122:123], v[84:85]
	v_pk_mul_f32 v[78:79], v[140:141], v[78:79]
	s_waitcnt vmcnt(11)
	v_mov_b64_e32 v[124:125], v[20:21]
	v_add_f32_e32 v88, v78, v79
	v_pk_mul_f32 v[78:79], v[86:87], v[84:85]
	v_mov_b64_e32 v[122:123], v[18:19]
	v_add_f32_e32 v78, v78, v79
	v_cvt_pk_bf16_f32 v105, v88, v78
	global_store_dwordx4 v[156:157], v[102:105], off offset:256
	ds_read_b128 v[84:87], v242 offset:5120
	ds_read_b128 v[98:101], v242 offset:4096
	s_nop 0
	ds_read_b128 v[102:105], v242 offset:13312
	ds_read_b128 v[116:119], v242 offset:12288
	v_pk_mul_f32 v[78:79], v[184:185], v[114:115]
	s_waitcnt lgkmcnt(2)
	v_mov_b32_e32 v88, v98
	v_lshlrev_b32_e32 v98, 16, v34
	s_waitcnt lgkmcnt(0)
	v_mov_b32_e32 v89, v116
	v_pk_mul_f32 v[78:79], v[78:79], v[88:89]
	v_pk_mul_f32 v[88:89], v[196:197], v[114:115]
	v_mov_b32_e32 v116, v99
	v_pk_mul_f32 v[88:89], v[88:89], v[116:117]
	v_pk_mul_f32 v[78:79], v[236:237], v[78:79]
	v_pk_mul_f32 v[74:75], v[74:75], v[88:89]
	v_add_f32_e32 v78, v78, v79
	v_add_f32_e32 v74, v74, v75
	v_cvt_pk_bf16_f32 v74, v78, v74
	v_pk_mul_f32 v[78:79], v[80:81], v[114:115]
	v_mov_b32_e32 v80, v100
	v_mov_b32_e32 v81, v118
	v_pk_mul_f32 v[78:79], v[78:79], v[80:81]
	v_pk_mul_f32 v[80:81], v[186:187], v[114:115]
	v_mov_b32_e32 v118, v101
	v_pk_mul_f32 v[80:81], v[80:81], v[118:119]
	v_pk_mul_f32 v[78:79], v[194:195], v[78:79]
	v_mov_b32_e32 v100, v111
	v_add_f32_e32 v75, v78, v79
	v_pk_mul_f32 v[78:79], v[226:227], v[80:81]
	v_mov_b32_e32 v80, v84
	v_add_f32_e32 v78, v78, v79
	v_cvt_pk_bf16_f32 v75, v75, v78
	v_pk_mul_f32 v[78:79], v[200:201], v[114:115]
	v_mov_b32_e32 v81, v102
	v_pk_mul_f32 v[78:79], v[78:79], v[80:81]
	v_pk_mul_f32 v[80:81], v[198:199], v[114:115]
	v_mov_b32_e32 v102, v85
	v_pk_mul_f32 v[80:81], v[80:81], v[102:103]
	v_pk_mul_f32 v[78:79], v[222:223], v[78:79]
	v_pk_mul_f32 v[76:77], v[76:77], v[80:81]
	v_add_f32_e32 v78, v78, v79
	v_add_f32_e32 v76, v76, v77
	v_cvt_pk_bf16_f32 v76, v78, v76
	v_pk_mul_f32 v[78:79], v[82:83], v[114:115]
	v_mov_b32_e32 v80, v86
	v_mov_b32_e32 v81, v104
	v_pk_mul_f32 v[78:79], v[78:79], v[80:81]
	v_pk_mul_f32 v[80:81], v[202:203], v[114:115]
	v_pk_mul_f32 v[78:79], v[208:209], v[78:79]
	v_mov_b32_e32 v104, v87
	v_add_f32_e32 v77, v78, v79
	v_mul_f32_e32 v78, 0xbfb8aa3b, v218
	v_mul_f32_e32 v79, 0xbfb8aa3b, v219
	v_exp_f32_e32 v78, v78
	v_exp_f32_e32 v79, v79
	v_pk_mul_f32 v[80:81], v[80:81], v[104:105]
	v_mov_b32_e32 v101, v113
	v_add_f32_e32 v78, 1.0, v78
	v_add_f32_e32 v79, 1.0, v79
	v_rcp_f32_e32 v78, v78
	v_rcp_f32_e32 v79, v79
	v_lshlrev_b32_e32 v99, 16, v38
	v_pk_mul_f32 v[100:101], v[100:101], v[114:115]
	v_mov_b32_e32 v111, v112
	v_pk_mul_f32 v[78:79], v[78:79], v[218:219]
	s_waitcnt vmcnt(9)
	v_mov_b64_e32 v[120:121], v[16:17]
	v_pk_mul_f32 v[78:79], v[78:79], v[80:81]
	v_mov_b64_e32 v[118:119], v[14:15]
	v_add_f32_e32 v78, v78, v79
	v_cvt_pk_bf16_f32 v77, v77, v78
	global_store_dwordx4 v[156:157], v[74:77], off offset:512
	ds_read_b128 v[74:77], v242 offset:7168
	s_nop 0
	ds_read_b128 v[82:85], v242 offset:6144
	ds_read_b128 v[78:81], v242 offset:15360
	ds_read_b128 v[86:89], v242 offset:14336
	s_waitcnt lgkmcnt(2)
	v_mov_b32_e32 v102, v82
	v_mul_f32_e32 v82, 0xbfb8aa3b, v98
	v_exp_f32_e32 v82, v82
	s_waitcnt lgkmcnt(0)
	v_mov_b32_e32 v103, v86
	v_pk_mul_f32 v[100:101], v[100:101], v[102:103]
	v_mov_b32_e32 v86, v83
	v_add_f32_e32 v82, 1.0, v82
	v_rcp_f32_e32 v102, v82
	v_mul_f32_e32 v82, 0xbfb8aa3b, v99
	v_exp_f32_e32 v82, v82
	s_nop 0
	v_add_f32_e32 v82, 1.0, v82
	v_rcp_f32_e32 v103, v82
	s_nop 0
	v_pk_mul_f32 v[98:99], v[102:103], v[98:99]
	s_nop 0
	v_pk_mul_f32 v[98:99], v[98:99], v[100:101]
	v_mov_b32_e32 v100, v107
	v_add_f32_e32 v102, v98, v99
	v_and_b32_e32 v98, 0xffff0000, v34
	v_mul_f32_e32 v34, 0xbfb8aa3b, v98
	v_exp_f32_e32 v34, v34
	v_mov_b32_e32 v101, v109
	v_and_b32_e32 v99, 0xffff0000, v38
	v_pk_mul_f32 v[100:101], v[100:101], v[114:115]
	v_add_f32_e32 v34, 1.0, v34
	v_pk_mul_f32 v[82:83], v[100:101], v[86:87]
	v_rcp_f32_e32 v86, v34
	v_mul_f32_e32 v34, 0xbfb8aa3b, v99
	v_exp_f32_e32 v34, v34
	v_mov_b32_e32 v107, v108
	v_add_f32_e32 v34, 1.0, v34
	v_rcp_f32_e32 v87, v34
	s_nop 0
	v_pk_mul_f32 v[86:87], v[86:87], v[98:99]
	s_nop 0
	v_pk_mul_f32 v[82:83], v[86:87], v[82:83]
	v_pk_mul_f32 v[86:87], v[110:111], v[114:115]
	v_add_f32_e32 v34, v82, v83
	v_lshlrev_b32_e32 v82, 16, v35
	v_mul_f32_e32 v38, 0xbfb8aa3b, v82
	v_exp_f32_e32 v38, v38
	v_lshlrev_b32_e32 v83, 16, v39
	v_mov_b32_e32 v98, v84
	v_mov_b32_e32 v99, v88
	v_add_f32_e32 v38, 1.0, v38
	v_pk_mul_f32 v[86:87], v[86:87], v[98:99]
	v_rcp_f32_e32 v98, v38
	v_mul_f32_e32 v38, 0xbfb8aa3b, v83
	v_exp_f32_e32 v38, v38
	v_and_b32_e32 v39, 0xffff0000, v39
	v_mov_b32_e32 v88, v85
	v_cvt_pk_bf16_f32 v34, v102, v34
	v_add_f32_e32 v38, 1.0, v38
	v_rcp_f32_e32 v99, v38
	v_and_b32_e32 v38, 0xffff0000, v35
	v_mul_f32_e32 v35, 0xbfb8aa3b, v38
	v_exp_f32_e32 v35, v35
	v_pk_mul_f32 v[82:83], v[98:99], v[82:83]
	s_waitcnt vmcnt(6)
	v_mov_b64_e32 v[112:113], v[24:25]
	v_pk_mul_f32 v[82:83], v[82:83], v[86:87]
	v_add_f32_e32 v35, 1.0, v35
	v_rcp_f32_e32 v84, v35
	v_mul_f32_e32 v35, 0xbfb8aa3b, v39
	v_exp_f32_e32 v35, v35
	v_add_f32_e32 v86, v82, v83
	v_pk_mul_f32 v[82:83], v[106:107], v[114:115]
	v_mov_b64_e32 v[108:109], v[28:29]
	v_add_f32_e32 v35, 1.0, v35
	v_rcp_f32_e32 v85, v35
	v_pk_mul_f32 v[82:83], v[82:83], v[88:89]
	v_mov_b64_e32 v[106:107], v[26:27]
	v_mov_b64_e32 v[110:111], v[22:23]
	v_pk_mul_f32 v[38:39], v[84:85], v[38:39]
	v_mov_b32_e32 v84, v74
	v_pk_mul_f32 v[38:39], v[38:39], v[82:83]
	v_mov_b32_e32 v82, v95
	v_add_f32_e32 v35, v38, v39
	v_lshlrev_b32_e32 v38, 16, v36
	v_mul_f32_e32 v74, 0xbfb8aa3b, v38
	v_exp_f32_e32 v74, v74
	v_mov_b32_e32 v83, v97
	v_lshlrev_b32_e32 v39, 16, v40
	v_pk_mul_f32 v[82:83], v[82:83], v[114:115]
	v_mov_b32_e32 v85, v78
	v_add_f32_e32 v74, 1.0, v74
	v_pk_mul_f32 v[82:83], v[82:83], v[84:85]
	v_rcp_f32_e32 v84, v74
	v_mul_f32_e32 v74, 0xbfb8aa3b, v39
	v_exp_f32_e32 v74, v74
	v_mov_b32_e32 v78, v75
	v_mov_b32_e32 v95, v96
	v_cvt_pk_bf16_f32 v35, v86, v35
	v_add_f32_e32 v74, 1.0, v74
	v_rcp_f32_e32 v85, v74
	v_mov_b64_e32 v[88:89], v[56:57]
	v_mov_b64_e32 v[86:87], v[54:55]
	v_pk_mul_f32 v[38:39], v[84:85], v[38:39]
	s_nop 0
	v_pk_mul_f32 v[38:39], v[38:39], v[82:83]
	v_mov_b32_e32 v82, v91
	v_add_f32_e32 v84, v38, v39
	v_and_b32_e32 v38, 0xffff0000, v36
	v_mul_f32_e32 v36, 0xbfb8aa3b, v38
	v_exp_f32_e32 v36, v36
	v_mov_b32_e32 v83, v93
	v_and_b32_e32 v39, 0xffff0000, v40
	v_pk_mul_f32 v[82:83], v[82:83], v[114:115]
	v_add_f32_e32 v36, 1.0, v36
	v_pk_mul_f32 v[74:75], v[82:83], v[78:79]
	v_rcp_f32_e32 v78, v36
	v_mul_f32_e32 v36, 0xbfb8aa3b, v39
	v_exp_f32_e32 v36, v36
	v_mov_b32_e32 v91, v92
	v_add_f32_e32 v36, 1.0, v36
	v_rcp_f32_e32 v79, v36
	s_nop 0
	v_pk_mul_f32 v[38:39], v[78:79], v[38:39]
	s_nop 0
	v_pk_mul_f32 v[38:39], v[38:39], v[74:75]
	v_pk_mul_f32 v[74:75], v[94:95], v[114:115]
	v_add_f32_e32 v36, v38, v39
	v_lshlrev_b32_e32 v38, 16, v37
	v_mul_f32_e32 v40, 0xbfb8aa3b, v38
	v_exp_f32_e32 v40, v40
	v_lshlrev_b32_e32 v39, 16, v41
	v_mov_b32_e32 v78, v76
	v_mov_b32_e32 v79, v80
	v_add_f32_e32 v40, 1.0, v40
	v_pk_mul_f32 v[74:75], v[74:75], v[78:79]
	v_rcp_f32_e32 v78, v40
	v_mul_f32_e32 v40, 0xbfb8aa3b, v39
	v_exp_f32_e32 v40, v40
	v_mov_b32_e32 v80, v77
	v_cvt_pk_bf16_f32 v36, v84, v36
	v_mov_b64_e32 v[84:85], v[52:53]
	v_add_f32_e32 v40, 1.0, v40
	v_rcp_f32_e32 v79, v40
	v_mov_b64_e32 v[96:97], v[44:45]
	v_mov_b64_e32 v[82:83], v[50:51]
	v_mov_b64_e32 v[94:95], v[42:43]
	v_pk_mul_f32 v[38:39], v[78:79], v[38:39]
	s_nop 0
	v_pk_mul_f32 v[38:39], v[38:39], v[74:75]
	s_nop 0
	v_add_f32_e32 v76, v38, v39
	v_and_b32_e32 v38, 0xffff0000, v37
	v_mul_f32_e32 v37, 0xbfb8aa3b, v38
	v_exp_f32_e32 v37, v37
	v_and_b32_e32 v39, 0xffff0000, v41
	v_pk_mul_f32 v[40:41], v[90:91], v[114:115]
	v_mov_b64_e32 v[92:93], v[48:49]
	v_add_f32_e32 v37, 1.0, v37
	v_rcp_f32_e32 v74, v37
	v_mul_f32_e32 v37, 0xbfb8aa3b, v39
	v_exp_f32_e32 v37, v37
	v_pk_mul_f32 v[40:41], v[40:41], v[80:81]
	v_mov_b64_e32 v[80:81], v[60:61]
	s_waitcnt vmcnt(5)
	v_mov_b64_e32 v[116:117], v[32:33]
	v_add_f32_e32 v37, 1.0, v37
	v_rcp_f32_e32 v75, v37
	v_mov_b64_e32 v[90:91], v[46:47]
	v_mov_b64_e32 v[78:79], v[58:59]
	v_mov_b64_e32 v[114:115], v[30:31]
	v_pk_mul_f32 v[38:39], v[74:75], v[38:39]
	s_nop 0
	v_pk_mul_f32 v[38:39], v[38:39], v[40:41]
	s_nop 0
	v_add_f32_e32 v37, v38, v39
	v_cvt_pk_bf16_f32 v37, v76, v37
	global_store_dwordx4 v[156:157], v[34:37], off offset:768
	v_mov_b64_e32 v[76:77], v[64:65]
	s_waitcnt vmcnt(4)
	v_mov_b64_e32 v[38:39], v[66:67]
	v_mov_b64_e32 v[34:35], v[70:71]
	v_lshl_add_u64 v[156:157], v[156:157], 0, s[12:13]
	v_mov_b64_e32 v[36:37], v[72:73]
	v_mov_b64_e32 v[74:75], v[62:63]
	v_mov_b64_e32 v[40:41], v[68:69]
	s_cbranch_scc1 .LBB0_530

.LBB0_1172:
	s_or_b64 exec, exec, s[4:5]
	s_and_b32 s4, s7, 0x3fffffc0
	s_lshl_b32 s4, s4, 2
	s_add_i32 s69, s4, 0
	s_lshl_b32 s4, s51, 12
	v_and_b32_e32 v154, 63, v151
	s_add_i32 s4, s4, 0
	v_lshlrev_b32_e32 v74, 4, v154
	s_add_i32 s4, s4, 0x1a800
	v_add_u32_e32 v158, s4, v74
	s_waitcnt vmcnt(0) lgkmcnt(0)
	ds_write_b128 v158, v[2:5]
	ds_write_b128 v158, v[6:9] offset:1024
	ds_write_b128 v158, v[10:13] offset:2048
	ds_write_b128 v158, v[14:17] offset:3072
	v_mov_b32_e32 v2, v154
	s_mul_i32 s30, s51, 0xc00
	v_lshlrev_b32_e32 v2, 4, v2
	v_add_u32_e32 v3, s30, v2
	v_mul_hi_i32 v4, v3, s60
	s_add_i32 s69, s69, 0x1a000
	v_lshrrev_b32_e32 v5, 31, v4
	v_ashrrev_i32_e32 v4, 6, v4
	s_cmp_lg_u32 0, -1
	s_mul_i32 s4, s74, 0x1080
	v_add_u32_e32 v4, v4, v5
	s_cselect_b32 s7, 0, 0
	s_mul_hi_i32 s5, s74, 0x1080
	s_add_u32 s4, s3, s4
	v_mad_i32_i24 v3, v4, s61, v3
	v_lshlrev_b32_e32 v5, 3, v4
	s_addc_u32 s5, s35, s5
	s_lshl_b32 s46, s8, 8
	v_bitop3_b32 v3, v3, v5, s62 bitop3:0x78
	v_lshrrev_b32_e32 v5, 1, v3
	v_mov_b32_e32 v75, s46
	v_cmp_gt_i32_e32 vcc, s59, v3
	v_mad_i32_i24 v4, v4, s63, v5
	s_add_i32 s10, s30, 0
	v_cndmask_b32_e32 v3, v148, v75, vcc
	v_add_lshl_u32 v3, v4, v3, 1
	s_add_i32 m0, s10, 0x8000
	s_add_i32 s31, s30, 0x400
	global_load_lds_dwordx4 v3, s[4:5]
	v_add_u32_e32 v3, s31, v2
	v_mul_hi_i32 v4, v3, s60
	v_lshrrev_b32_e32 v5, 31, v4
	v_ashrrev_i32_e32 v4, 6, v4
	v_add_u32_e32 v4, v4, v5
	v_mad_i32_i24 v3, v4, s61, v3
	v_lshlrev_b32_e32 v5, 3, v4
	v_bitop3_b32 v3, v3, v5, s62 bitop3:0x78
	v_lshrrev_b32_e32 v5, 1, v3
	v_cmp_gt_i32_e32 vcc, s59, v3
	v_mad_i32_i24 v4, v4, s63, v5
	s_add_i32 s36, s30, 0x800
	v_cndmask_b32_e32 v3, v148, v75, vcc
	v_add_lshl_u32 v3, v4, v3, 1
	s_add_i32 m0, s10, 0x8400
	v_add_u32_e32 v2, s36, v2
	global_load_lds_dwordx4 v3, s[4:5]
	v_mul_hi_i32 v3, v2, s60
	v_lshrrev_b32_e32 v4, 31, v3
	v_ashrrev_i32_e32 v3, 6, v3
	v_add_u32_e32 v3, v3, v4
	v_mad_i32_i24 v2, v3, s61, v2
	v_lshlrev_b32_e32 v4, 3, v3
	v_bitop3_b32 v2, v2, v4, s62 bitop3:0x78
	v_lshrrev_b32_e32 v4, 1, v2
	v_cmp_gt_i32_e32 vcc, s59, v2
	v_mad_i32_i24 v3, v3, s63, v4
	s_add_i32 m0, s10, 0x8800
	v_cndmask_b32_e32 v2, v148, v75, vcc
	v_add_lshl_u32 v2, v3, v2, 1
	global_load_lds_dwordx4 v2, s[4:5]
	v_mov_b32_e32 v2, v154
	s_lshl_b32 s37, s51, 11
	v_lshlrev_b32_e32 v4, 4, v2
	v_lshlrev_b32_e32 v3, 3, v2
	v_bfe_u32 v5, v2, 2, 2
	v_lshrrev_b32_e32 v6, 1, v2
	v_and_or_b32 v5, v6, 8, v5
	v_and_or_b32 v6, v3, 24, s46
	v_add_u32_e32 v3, s37, v4
	v_ashrrev_i32_e32 v3, 8, v3
	v_and_b32_e32 v7, 0x3fffff0, v3
	v_lshrrev_b32_e32 v3, 1, v3
	v_and_b32_e32 v3, 4, v3
	v_or3_b32 v3, v7, v3, v5
	v_and_or_b32 v2, v2, s64, v6
	v_mad_u64_u32 v[2:3], s[8:9], v3, s63, v[2:3]
	s_add_i32 s70, s37, 0
	v_lshl_add_u32 v2, v2, 1, v149
	s_mov_b32 m0, s70
	s_or_b32 s71, s37, 0x400
	global_load_lds_dwordx4 v2, s[4:5]
	v_add_u32_e32 v2, s71, v4
	v_ashrrev_i32_e32 v3, 8, v2
	v_and_b32_e32 v4, 0x3fffff0, v3
	v_lshrrev_b32_e32 v3, 1, v3
	v_and_b32_e32 v3, 4, v3
	v_lshrrev_b32_e32 v2, 4, v2
	v_or3_b32 v3, v4, v3, v5
	v_and_or_b32 v2, v2, s64, v6
	v_mad_u64_u32 v[2:3], s[8:9], v3, s63, v[2:3]
	s_add_i32 s72, s70, 0x400
	v_lshl_add_u32 v2, v2, 1, v149
	s_mov_b32 m0, s72
	v_mad_u32_u24 v58, v152, s54, 0
	global_load_lds_dwordx4 v2, s[4:5]
	v_mov_b32_e32 v2, v154
	s_or_b32 s4, s74, 64
	v_lshlrev_b32_e32 v2, 4, v2
	v_add_u32_e32 v3, s30, v2
	v_mul_hi_i32 v4, v3, s60
	v_lshrrev_b32_e32 v5, 31, v4
	v_ashrrev_i32_e32 v4, 6, v4
	v_add_u32_e32 v4, v4, v5
	v_mad_i32_i24 v3, v4, s61, v3
	v_lshlrev_b32_e32 v5, 3, v4
	v_bitop3_b32 v3, v3, v5, s62 bitop3:0x78
	s_mul_hi_i32 s5, s4, 0x1080
	s_mulk_i32 s4, 0x1080
	v_lshrrev_b32_e32 v5, 1, v3
	v_cmp_gt_i32_e32 vcc, s59, v3
	s_add_u32 s4, s3, s4
	v_mad_i32_i24 v4, v4, s63, v5
	v_cndmask_b32_e32 v3, v148, v75, vcc
	s_addc_u32 s5, s35, s5
	v_add_lshl_u32 v3, v4, v3, 1
	s_add_i32 m0, s10, 0xe000
	s_add_i32 s76, s70, 0x4000
	global_load_lds_dwordx4 v3, s[4:5]
	v_add_u32_e32 v3, s31, v2
	v_mul_hi_i32 v4, v3, s60
	v_lshrrev_b32_e32 v5, 31, v4
	v_ashrrev_i32_e32 v4, 6, v4
	v_add_u32_e32 v4, v4, v5
	v_mad_i32_i24 v3, v4, s61, v3
	v_lshlrev_b32_e32 v5, 3, v4
	v_bitop3_b32 v3, v3, v5, s62 bitop3:0x78
	v_lshrrev_b32_e32 v5, 1, v3
	v_cmp_gt_i32_e32 vcc, s59, v3
	v_mad_i32_i24 v4, v4, s63, v5
	s_add_i32 m0, s10, 0xe400
	v_cndmask_b32_e32 v3, v148, v75, vcc
	v_add_lshl_u32 v3, v4, v3, 1
	v_add_u32_e32 v2, s36, v2
	global_load_lds_dwordx4 v3, s[4:5]
	v_mul_hi_i32 v3, v2, s60
	v_lshrrev_b32_e32 v4, 31, v3
	v_ashrrev_i32_e32 v3, 6, v3
	v_add_u32_e32 v3, v3, v4
	v_mad_i32_i24 v2, v3, s61, v2
	v_lshlrev_b32_e32 v4, 3, v3
	v_bitop3_b32 v2, v2, v4, s62 bitop3:0x78
	v_lshrrev_b32_e32 v4, 1, v2
	v_cmp_gt_i32_e32 vcc, s59, v2
	v_mad_i32_i24 v3, v3, s63, v4
	s_add_i32 m0, s10, 0xe800
	v_cndmask_b32_e32 v2, v148, v75, vcc
	v_add_lshl_u32 v2, v3, v2, 1
	global_load_lds_dwordx4 v2, s[4:5]
	v_mov_b32_e32 v2, v154
	s_mov_b32 m0, s76
	v_lshlrev_b32_e32 v4, 4, v2
	v_lshlrev_b32_e32 v3, 3, v2
	v_bfe_u32 v5, v2, 2, 2
	v_lshrrev_b32_e32 v6, 1, v2
	v_and_or_b32 v5, v6, 8, v5
	v_and_or_b32 v6, v3, 24, s46
	v_add_u32_e32 v3, s37, v4
	v_ashrrev_i32_e32 v3, 8, v3
	v_and_b32_e32 v7, 0x3fffff0, v3
	v_lshrrev_b32_e32 v3, 1, v3
	v_and_b32_e32 v3, 4, v3
	v_or3_b32 v3, v7, v3, v5
	v_and_or_b32 v2, v2, s64, v6
	v_mad_u64_u32 v[2:3], s[8:9], v3, s63, v[2:3]
	v_lshl_add_u32 v2, v2, 1, v149
	global_load_lds_dwordx4 v2, s[4:5]
	v_add_u32_e32 v2, s71, v4
	v_ashrrev_i32_e32 v3, 8, v2
	v_and_b32_e32 v4, 0x3fffff0, v3
	v_lshrrev_b32_e32 v3, 1, v3
	v_and_b32_e32 v3, 4, v3
	v_lshrrev_b32_e32 v2, 4, v2
	v_or3_b32 v3, v4, v3, v5
	v_and_or_b32 v2, v2, s64, v6
	v_mad_u64_u32 v[2:3], s[8:9], v3, s63, v[2:3]
	s_add_i32 s77, s70, 0x4400
	v_lshl_add_u32 v2, v2, 1, v149
	s_mov_b32 m0, s77
	v_bfe_u32 v18, v151, 1, 3
	v_xor_b32_e32 v18, v153, v18
	global_load_lds_dwordx4 v2, s[4:5]
	v_lshl_add_u32 v159, v18, 4, v58
	s_waitcnt vmcnt(0) lgkmcnt(0)
	s_barrier
	ds_read_b128 v[2:5], v159 offset:32768
	ds_read_b128 v[6:9], v159 offset:32896
	s_waitcnt lgkmcnt(0)
	v_mfma_f32_32x32x16_bf16 v[34:49], v[2:5], v[126:129], 0
	ds_read_b128 v[2:5], v159 offset:45056
	v_bfe_u32 v59, v151, 1, 3
	v_bitop3_b32 v10, v153, v59, 2 bitop3:0x36
	v_lshl_add_u32 v161, v10, 4, v58
	ds_read_b128 v[10:13], v159 offset:33024
	v_bitop3_b32 v50, v153, v59, 4 bitop3:0x36
	v_lshl_add_u32 v162, v50, 4, v58
	s_waitcnt lgkmcnt(0)
	v_mfma_f32_32x32x16_bf16 v[18:33], v[2:5], v[126:129], 0
	ds_read_b128 v[2:5], v161 offset:32768
	ds_read_b128 v[14:17], v161 offset:32896
	ds_read_b128 v[50:53], v161 offset:33024
	v_bitop3_b32 v59, v153, v59, 6 bitop3:0x36
	v_lshl_add_u32 v163, v59, 4, v58
	s_or_b32 s4, s74, 0x80
	s_mul_hi_i32 s5, s4, 0x1080
	s_mulk_i32 s4, 0x1080
	s_waitcnt lgkmcnt(0)
	v_mfma_f32_32x32x16_bf16 v[34:49], v[2:5], v[122:125], v[34:49]
	ds_read_b128 v[2:5], v161 offset:45056
	s_add_u32 s4, s3, s4
	s_addc_u32 s5, s35, s5
	s_add_i32 m0, s66, s30
	s_mov_b32 s8, 0
	s_mov_b32 s9, s8
	s_mov_b32 s10, s8
	s_waitcnt lgkmcnt(0)
	v_mfma_f32_32x32x16_bf16 v[18:33], v[2:5], v[122:125], v[18:33]
	ds_read_b128 v[2:5], v162 offset:32768
	ds_read_b128 v[54:57], v162 offset:32896
	ds_read_b128 v[58:61], v162 offset:33024
	s_mov_b32 s11, s8
	s_mov_b32 s12, s8
	s_mov_b32 s13, s8
	s_mov_b32 s14, s8
	s_mov_b32 s15, s8
	s_waitcnt lgkmcnt(0)
	v_mfma_f32_32x32x16_bf16 v[34:49], v[2:5], v[118:121], v[34:49]
	ds_read_b128 v[2:5], v162 offset:45056
	s_mov_b32 s16, s8
	s_mov_b32 s17, s8
	s_mov_b32 s18, s8
	s_mov_b32 s19, s8
	s_mov_b32 s20, s8
	s_mov_b32 s21, s8
	s_waitcnt lgkmcnt(0)
	v_mfma_f32_32x32x16_bf16 v[18:33], v[2:5], v[118:121], v[18:33]
	ds_read_b128 v[2:5], v163 offset:32768
	ds_read_b128 v[62:65], v163 offset:32896
	s_mov_b32 s22, s8
	s_mov_b32 s23, s8
	s_mov_b32 s78, 2
	s_mov_b32 s79, 4
	s_mov_b32 s80, 3
	s_mov_b32 s81, 1
	s_waitcnt lgkmcnt(0)
	v_mfma_f32_32x32x16_bf16 v[34:49], v[2:5], v[114:117], v[34:49]
	ds_read_b128 v[2:5], v163 offset:45056
	ds_read_b128 v[66:69], v163 offset:33024
	v_lshl_add_u32 v155, v152, 2, s69
	v_mov_b32_e32 v157, 0
	s_waitcnt lgkmcnt(0)
	v_mfma_f32_32x32x16_bf16 v[18:33], v[2:5], v[114:117], v[18:33]
	v_mfma_f32_32x32x16_bf16 v[34:49], v[6:9], v[110:113], v[34:49]
	ds_read_b128 v[2:5], v159 offset:45184
	ds_read_b128 v[6:9], v159 offset:45312
	s_waitcnt lgkmcnt(0)
	v_mfma_f32_32x32x16_bf16 v[18:33], v[2:5], v[110:113], v[18:33]
	v_mfma_f32_32x32x16_bf16 v[34:49], v[14:17], v[106:109], v[34:49]
	ds_read_b128 v[2:5], v161 offset:45184
	ds_read_b128 v[14:17], v161 offset:45312
	s_waitcnt lgkmcnt(0)
	v_mfma_f32_32x32x16_bf16 v[18:33], v[2:5], v[106:109], v[18:33]
	v_mfma_f32_32x32x16_bf16 v[34:49], v[54:57], v[102:105], v[34:49]
	ds_read_b128 v[2:5], v162 offset:45184
	ds_read_b128 v[54:57], v162 offset:45312
	s_waitcnt lgkmcnt(0)
	v_mfma_f32_32x32x16_bf16 v[18:33], v[2:5], v[102:105], v[18:33]
	v_mfma_f32_32x32x16_bf16 v[34:49], v[62:65], v[98:101], v[34:49]
	ds_read_b128 v[2:5], v163 offset:45184
	ds_read_b128 v[62:65], v163 offset:45312
	s_waitcnt lgkmcnt(0)
	v_mfma_f32_32x32x16_bf16 v[18:33], v[2:5], v[98:101], v[18:33]
	ds_read_b128 v[2:5], v158
	ds_read_b128 v[70:73], v158 offset:1024
	s_waitcnt lgkmcnt(0)
	v_mfma_f32_32x32x16_bf16 v[34:49], v[10:13], v[2:5], v[34:49]
	v_mfma_f32_32x32x16_bf16 v[18:33], v[6:9], v[2:5], v[18:33]
	ds_read_b128 v[2:5], v158 offset:2048
	v_lshlrev_b32_e32 v6, 3, v154
	v_and_b32_e32 v7, 0xc0, v74
	v_lshlrev_b32_e32 v8, 1, v154
	v_and_or_b32 v7, v6, 24, v7
	v_and_b32_e32 v8, 32, v8
	v_and_b32_e32 v6, 0x100, v6
	v_mfma_f32_32x32x16_bf16 v[34:49], v[50:53], v[70:73], v[34:49]
	ds_read_b128 v[50:53], v158 offset:3072
	s_waitcnt lgkmcnt(0)
	s_barrier
	v_bfe_u32 v232, v154, 2, 2
	v_lshrrev_b32_e32 v254, 1, v154
	v_and_or_b32 v232, v254, 8, v232
	v_lshlrev_b32_e32 v254, 3, v154
	v_and_or_b32 v251, v254, 24, s46
	v_lshl_add_u32 v254, v154, 4, s37
	v_ashrrev_i32_e32 v254, 8, v254
	v_and_b32_e32 v252, 0x3fffff0, v254
	v_lshrrev_b32_e32 v254, 1, v254
	v_and_b32_e32 v254, 4, v254
	v_or3_b32 v254, v252, v254, v232
	v_and_or_b32 v252, v154, s64, v251
	v_mad_u32_u24 v252, v254, s63, v252
	v_lshl_add_u32 v253, v252, 1, v149
	v_lshl_add_u32 v254, v154, 4, s71
	v_ashrrev_i32_e32 v252, 8, v254
	v_lshrrev_b32_e32 v254, 4, v254
	v_and_or_b32 v254, v254, s64, v251
	v_and_b32_e32 v251, 0x3fffff0, v252
	v_lshrrev_b32_e32 v252, 1, v252
	v_and_b32_e32 v252, 4, v252
	v_or3_b32 v252, v251, v252, v232
	v_mad_u32_u24 v254, v252, s63, v254
	v_lshl_add_u32 v254, v254, 1, v149
	v_mfma_f32_32x32x16_bf16 v[18:33], v[14:17], v[70:73], v[18:33]
	s_waitcnt lgkmcnt(0)
	v_mfma_f32_32x32x16_bf16 v[34:49], v[58:61], v[2:5], v[34:49]
	v_or3_b32 v58, v7, v8, v6
	v_add_u32_e32 v160, s7, v58
	v_mfma_f32_32x32x16_bf16 v[18:33], v[54:57], v[2:5], v[18:33]
	v_mov_b64_e32 v[2:3], s[8:9]
	v_mov_b64_e32 v[4:5], s[10:11]
	v_mov_b64_e32 v[6:7], s[12:13]
	v_mov_b64_e32 v[8:9], s[14:15]
	v_mov_b64_e32 v[10:11], s[16:17]
	v_mov_b64_e32 v[12:13], s[18:19]
	v_mov_b64_e32 v[14:15], s[20:21]
	v_mfma_f32_32x32x16_bf16 v[34:49], v[66:69], v[50:53], v[34:49]
	v_mov_b64_e32 v[16:17], s[22:23]
	s_add_i32 s14, s75, -1
	s_movk_i32 s9, 0x80
	s_mov_b32 s16, 0xc000
	v_mfma_f32_32x32x16_bf16 v[18:33], v[62:65], v[50:53], v[18:33]
	s_nop 6
	v_max_f32_e32 v50, v35, v35
	v_max_f32_e32 v51, v34, v34
	v_max_f32_e32 v50, v51, v50
	v_mov_b32_e32 v51, v154
	v_max3_f32 v50, v50, v36, v37
	v_lshlrev_b32_e32 v51, 4, v51
	v_add_u32_e32 v52, s30, v51
	v_mul_hi_i32 v53, v52, s60
	v_lshrrev_b32_e32 v54, 31, v53
	v_ashrrev_i32_e32 v53, 6, v53
	v_add_u32_e32 v53, v53, v54
	v_mad_i32_i24 v52, v53, s61, v52
	v_lshlrev_b32_e32 v54, 3, v53
	v_bitop3_b32 v52, v52, v54, s62 bitop3:0x78
	v_lshrrev_b32_e32 v54, 1, v52
	v_cmp_gt_i32_e32 vcc, s59, v52
	v_mad_i32_i24 v53, v53, s63, v54
	v_max3_f32 v50, v50, v38, v39
	v_cndmask_b32_e32 v52, v148, v75, vcc
	v_add_lshl_u32 v52, v53, v52, 1
	v_mov_b32_e32 v232, v52
	global_load_lds_dwordx4 v52, s[4:5]
	v_add_u32_e32 v52, s31, v51
	v_mul_hi_i32 v53, v52, s60
	v_lshrrev_b32_e32 v54, 31, v53
	v_ashrrev_i32_e32 v53, 6, v53
	v_add_u32_e32 v53, v53, v54
	v_mad_i32_i24 v52, v53, s61, v52
	v_lshlrev_b32_e32 v54, 3, v53
	v_bitop3_b32 v52, v52, v54, s62 bitop3:0x78
	v_lshrrev_b32_e32 v54, 1, v52
	v_cmp_gt_i32_e32 vcc, s59, v52
	v_mad_i32_i24 v53, v53, s63, v54
	s_add_i32 m0, s66, s31
	v_cndmask_b32_e32 v52, v148, v75, vcc
	v_add_lshl_u32 v52, v53, v52, 1
	v_add_u32_e32 v51, s36, v51
	v_mov_b32_e32 v251, v52
	global_load_lds_dwordx4 v52, s[4:5]
	v_mul_hi_i32 v52, v51, s60
	v_lshrrev_b32_e32 v53, 31, v52
	v_ashrrev_i32_e32 v52, 6, v52
	v_add_u32_e32 v52, v52, v53
	v_mad_i32_i24 v51, v52, s61, v51
	v_lshlrev_b32_e32 v53, 3, v52
	v_bitop3_b32 v51, v51, v53, s62 bitop3:0x78
	v_lshrrev_b32_e32 v53, 1, v51
	v_cmp_gt_i32_e32 vcc, s59, v51
	v_mad_i32_i24 v52, v52, s63, v53
	s_add_i32 m0, s66, s36
	v_cndmask_b32_e32 v51, v148, v75, vcc
	v_add_lshl_u32 v51, v52, v51, 1
	v_mov_b32_e32 v252, v51
	global_load_lds_dwordx4 v51, s[4:5]
	v_max3_f32 v50, v50, v40, v41
	v_max3_f32 v50, v50, v42, v43
	v_max3_f32 v50, v50, v44, v45
	v_max3_f32 v50, v50, v46, v47
	v_max3_f32 v50, v50, v48, v49
	v_max3_f32 v50, v50, v18, v19
	v_max3_f32 v50, v50, v20, v21
	v_max3_f32 v50, v50, v22, v23
	v_max3_f32 v50, v50, v24, v25
	v_max3_f32 v50, v50, v26, v27
	v_max3_f32 v50, v50, v28, v29
	v_max3_f32 v50, v50, v30, v31
	v_max3_f32 v50, v50, v32, v33
	v_mov_b32_e32 v51, v50
	s_nop 1
	v_permlane32_swap_b32_e32 v50, v51
	v_max_f32_e32 v51, v51, v51
	v_max_f32_e32 v50, v50, v50
	v_max_f32_e32 v50, v50, v51
	v_add_f32_e32 v51, 0x7149f2ca, v50
	v_cmp_ge_f32_e32 vcc, s65, v51
	s_cmp_eq_u64 vcc, exec
	v_max_f32_e32 v51, 0xf149f2ca, v50
	s_cselect_b64 vcc, -1, 0
	v_cndmask_b32_e32 v165, v51, v150, vcc
	v_mul_f32_e32 v50, 0xbdd53b94, v165
	v_fmamk_f32 v34, v34, 0x3dd53b94, v50
	v_exp_f32_e32 v178, v34
	v_fmamk_f32 v34, v35, 0x3dd53b94, v50
	v_exp_f32_e32 v182, v34
	v_fmamk_f32 v34, v36, 0x3dd53b94, v50
	v_exp_f32_e32 v179, v34
	v_fmamk_f32 v34, v37, 0x3dd53b94, v50
	v_exp_f32_e32 v183, v34
	v_fmamk_f32 v34, v38, 0x3dd53b94, v50
	v_exp_f32_e32 v180, v34
	v_fmamk_f32 v34, v39, 0x3dd53b94, v50
	v_exp_f32_e32 v184, v34
	v_fmamk_f32 v34, v40, 0x3dd53b94, v50
	v_exp_f32_e32 v177, v34
	v_fmamk_f32 v34, v41, 0x3dd53b94, v50
	v_exp_f32_e32 v181, v34
	v_fmamk_f32 v34, v42, 0x3dd53b94, v50
	v_exp_f32_e32 v171, v34
	v_fmamk_f32 v34, v43, 0x3dd53b94, v50
	v_exp_f32_e32 v175, v34
	v_fmamk_f32 v34, v44, 0x3dd53b94, v50
	v_exp_f32_e32 v172, v34
	v_fmamk_f32 v34, v45, 0x3dd53b94, v50
	v_exp_f32_e32 v176, v34
	v_fmamk_f32 v34, v46, 0x3dd53b94, v50
	v_pk_fma_f32 v[140:141], v[24:25], s[48:49], v[50:51] op_sel_hi:[1,0,0]
	v_sub_f32_e32 v24, 0xf149f2ca, v51
	v_exp_f32_e32 v168, v34
	v_fmamk_f32 v34, v47, 0x3dd53b94, v50
	v_mul_f32_e32 v24, 0x3dd53b94, v24
	v_exp_f32_e32 v173, v34
	v_fmamk_f32 v34, v48, 0x3dd53b94, v50
	v_exp_f32_e32 v24, v24
	v_exp_f32_e32 v169, v34
	v_fmamk_f32 v34, v49, 0x3dd53b94, v50
	v_exp_f32_e32 v174, v34
	s_addk_i32 s7, 0x4000
	v_pk_fma_f32 v[130:131], v[32:33], s[48:49], v[50:51] op_sel_hi:[1,0,0]
	v_pk_fma_f32 v[132:133], v[30:31], s[48:49], v[50:51] op_sel_hi:[1,0,0]
	v_pk_fma_f32 v[136:137], v[28:29], s[48:49], v[50:51] op_sel_hi:[1,0,0]
	v_pk_fma_f32 v[138:139], v[26:27], s[48:49], v[50:51] op_sel_hi:[1,0,0]
	v_pk_fma_f32 v[142:143], v[22:23], s[48:49], v[50:51] op_sel_hi:[1,0,0]
	v_pk_fma_f32 v[144:145], v[20:21], s[48:49], v[50:51] op_sel_hi:[1,0,0]
	v_pk_fma_f32 v[146:147], v[18:19], s[48:49], v[50:51] op_sel_hi:[1,0,0]
	v_cndmask_b32_e64 v164, v24, 1.0, vcc
	v_add_u32_e32 v156, s7, v58
	v_mov_b64_e32 v[64:65], v[16:17]
	v_mov_b64_e32 v[48:49], v[16:17]
	v_mov_b64_e32 v[32:33], v[16:17]
	s_or_b32 s15, s6, 0x300
	v_cmp_gt_u32_e64 s[4:5], 32, v154
	s_movk_i32 s6, 0x6000
	v_mov_b64_e32 v[62:63], v[14:15]
	v_mov_b64_e32 v[60:61], v[12:13]
	v_mov_b64_e32 v[58:59], v[10:11]
	v_mov_b64_e32 v[56:57], v[8:9]
	v_mov_b64_e32 v[54:55], v[6:7]
	v_mov_b64_e32 v[52:53], v[4:5]
	v_mov_b64_e32 v[50:51], v[2:3]
	v_mov_b64_e32 v[46:47], v[14:15]
	v_mov_b64_e32 v[44:45], v[12:13]
	v_mov_b64_e32 v[42:43], v[10:11]
	v_mov_b64_e32 v[40:41], v[8:9]
	v_mov_b64_e32 v[38:39], v[6:7]
	v_mov_b64_e32 v[36:37], v[4:5]
	v_mov_b64_e32 v[34:35], v[2:3]
	v_mov_b64_e32 v[30:31], v[14:15]
	v_mov_b64_e32 v[28:29], v[12:13]
	v_mov_b64_e32 v[26:27], v[10:11]
	v_mov_b64_e32 v[24:25], v[8:9]
	v_mov_b64_e32 v[22:23], v[6:7]
	v_mov_b64_e32 v[20:21], v[4:5]
	v_mov_b64_e32 v[18:19], v[2:3]

.LBB0_2587:
	s_cmp_lt_i32 s92, 34
	s_cselect_b64 s[4:5], -1, 0
	s_cmp_gt_i32 s93, 33
	s_cselect_b64 s[6:7], -1, 0
	s_and_b64 s[4:5], s[4:5], s[6:7]
	s_andn2_b64 vcc, exec, s[4:5]
	s_cbranch_vccnz .LBB0_2641
	s_lshl_b32 s3, s89, 3
	s_add_i32 s3, s88, s3
	s_add_i32 s6, s3, 0x400
	s_cmpk_gt_i32 s6, 0x43ff
	s_mov_b32 s10, 13
	s_mov_b32 s4, 14
	s_cbranch_scc1 .LBB0_2591
	s_add_u32 s3, s26, 0x2a500000
	s_addc_u32 s15, s27, 0
	s_ashr_i32 s11, s10, 31
	s_lshl_b32 s8, s34, 3
	s_lshl_b64 s[10:11], s[10:11], 3
	s_add_u32 s12, s0, s10
	s_addc_u32 s13, s1, s11
	s_add_u32 s16, s26, 0x3d700000
	s_addc_u32 s17, s27, 0
	s_ashr_i32 s7, s6, 31
	s_lshl_b64 s[18:19], s[6:7], 12
	s_add_u32 s20, s16, s18
	s_addc_u32 s21, s17, s19
	s_add_u32 s22, s26, 0x41b00000
	s_waitcnt vmcnt(0)
	v_lshlrev_b32_e32 v2, 3, v250
	s_addc_u32 s23, s27, 0
	v_lshlrev_b32_e32 v1, 5, v250
	v_and_b32_e32 v2, 0x78, v2
	s_movk_i32 s5, 0xfe00
	s_add_u32 s28, s22, s18
	v_and_or_b32 v146, v1, s5, v2
	s_addc_u32 s29, s23, s19
	s_lshl_b64 s[10:11], s[6:7], 13
	v_ashrrev_i32_e32 v147, 31, v146
	s_add_u32 s10, s3, s10
	s_addc_u32 s11, s15, s11
	v_lshlrev_b64 v[2:3], 1, v[146:147]
	v_lshl_add_u64 v[4:5], s[10:11], 0, v[2:3]
	s_movk_i32 s7, 0x1000
	s_mov_b64 s[10:11], 0x1000
	v_lshl_add_u64 v[10:11], s[20:21], 0, v[2:3]
	v_add_co_u32_e32 v12, vcc, s7, v4
	v_lshl_add_u64 v[6:7], v[4:5], 0, s[10:11]
	v_lshl_add_u64 v[8:9], s[28:29], 0, v[2:3]
	global_load_dwordx4 v[34:37], v[4:5], off offset:768
	global_load_dwordx4 v[74:77], v[4:5], off offset:512
	global_load_dwordx4 v[78:81], v[6:7], off offset:512
	global_load_dwordx4 v[82:85], v[6:7], off offset:256
	global_load_dwordx4 v[106:109], v[8:9], off offset:512
	global_load_dwordx4 v[122:125], v[8:9], off offset:256
	global_load_dwordx4 v[118:121], v[10:11], off offset:512
	global_load_dwordx4 v[126:129], v[10:11], off offset:256
	v_addc_co_u32_e32 v13, vcc, 0, v5, vcc
	global_load_dwordx4 v[110:113], v[10:11], off offset:768
	global_load_dwordx4 v[94:97], v[12:13], off
	global_load_dwordx4 v[86:89], v[4:5], off offset:256
	global_load_dwordx4 v[90:93], v[4:5], off
	global_load_dwordx4 v[38:41], v[6:7], off offset:768
	global_load_dwordx4 v[130:133], v[8:9], off
	global_load_dwordx4 v[114:117], v[8:9], off offset:768
	global_load_dwordx4 v[134:137], v[10:11], off
	s_ashr_i32 s5, s4, 31
	s_lshl_b64 s[4:5], s[4:5], 3
	s_add_u32 s4, s0, s4
	s_addc_u32 s5, s1, s5
	s_load_dwordx2 s[12:13], s[12:13], 0x0
	s_nop 0
	s_load_dwordx2 s[4:5], s[4:5], 0x0
	v_lshlrev_b64 v[4:5], 2, v[146:147]
	v_lshl_add_u64 v[148:149], s[16:17], 0, v[2:3]
	v_lshl_add_u64 v[150:151], s[22:23], 0, v[2:3]
	s_waitcnt lgkmcnt(0)
	v_lshl_add_u64 v[6:7], s[12:13], 0, v[4:5]
	v_lshl_add_u64 v[4:5], s[4:5], 0, v[4:5]
	s_add_u32 s4, s26, s18
	s_addc_u32 s5, s27, s19
	s_mov_b64 s[12:13], 0x2000
	v_lshl_add_u64 v[2:3], s[4:5], 0, v[2:3]
	s_mov_b64 s[4:5], 0x45f00000
	s_ashr_i32 s9, s8, 31
	v_lshl_add_u64 v[152:153], v[6:7], 0, s[12:13]
	v_lshl_add_u64 v[154:155], v[4:5], 0, s[12:13]
	v_lshl_add_u64 v[156:157], v[2:3], 0, s[4:5]
	s_lshl_b64 s[12:13], s[8:9], 12
	s_mov_b32 s14, 0x3b000000
	v_mov_b32_e32 v1, 0x358637bd
	s_mov_b32 s9, 0xf800000
	v_mov_b32_e32 v171, 0x260
	v_lshlrev_b32_e32 v242, 4, v250
	s_lshl_b32 s98, s88, 14
	v_add_u32_e32 v242, s98, v242
	global_load_dwordx4 v[2:5], v[152:153], off
	global_load_dwordx4 v[6:9], v[152:153], off offset:16
	global_load_dwordx4 v[10:13], v[152:153], off offset:512
	global_load_dwordx4 v[14:17], v[152:153], off offset:528
	global_load_dwordx4 v[18:21], v[152:153], off offset:1024
	global_load_dwordx4 v[22:25], v[152:153], off offset:1040
	global_load_dwordx4 v[26:29], v[152:153], off offset:1536
	global_load_dwordx4 v[30:33], v[152:153], off offset:1552
	global_load_dwordx4 v[42:45], v[154:155], off
	global_load_dwordx4 v[46:49], v[154:155], off offset:16
	global_load_dwordx4 v[50:53], v[154:155], off offset:512
	global_load_dwordx4 v[54:57], v[154:155], off offset:528
	global_load_dwordx4 v[58:61], v[154:155], off offset:1024
	global_load_dwordx4 v[62:65], v[154:155], off offset:1040
	global_load_dwordx4 v[66:69], v[154:155], off offset:1536
	global_load_dwordx4 v[70:73], v[154:155], off offset:1552
	s_waitcnt vmcnt(0)
	ds_write_b128 v242, v[2:5]
	ds_write_b128 v242, v[6:9] offset:1024
	ds_write_b128 v242, v[10:13] offset:2048
	ds_write_b128 v242, v[14:17] offset:3072
	ds_write_b128 v242, v[18:21] offset:4096
	ds_write_b128 v242, v[22:25] offset:5120
	ds_write_b128 v242, v[26:29] offset:6144
	ds_write_b128 v242, v[30:33] offset:7168
	ds_write_b128 v242, v[42:45] offset:8192
	ds_write_b128 v242, v[46:49] offset:9216
	ds_write_b128 v242, v[50:53] offset:10240
	ds_write_b128 v242, v[54:57] offset:11264
	ds_write_b128 v242, v[58:61] offset:12288
	ds_write_b128 v242, v[62:65] offset:13312
	ds_write_b128 v242, v[66:69] offset:14336
	ds_write_b128 v242, v[70:73] offset:15360
	s_waitcnt lgkmcnt(0)
